# v21 + nt hint on norm2's single-use reads of the bf16 residual stream
# baseline (speedup 1.0000x reference)
; #define GAS __attribute__((address_space(1)))
;     ...
;     for (int blk = blockIdx.x; blk < M / 32; blk += F.G) {
;         const int b = (blk * 32) >> 11;
;         __syncthreads();
;         for (int i = F.tid; i < DM / 4; i += NWAVES * 64) { const f32x4 g = ((const GAS f32x4*)gain)[i], sh = ((const GAS f32x4*)(F.MOD + b * MODW + sh_off))[i], sc = ((const GAS f32x4*)(F.MOD + b * MODW + sc_off))[i];
;             CA[i] = g * (sc + 1.0f); CB[i] = sh; }
;         __syncthreads();
;         const int m0 = blk * 32 + 4 * F.wave;
;         f32x4 va[16], vb[16];
.LBB0_2292:
	v_add_co_u32_e32 v20, vcc, 0x4000, v10
	global_load_dwordx4 v[16:19], v[10:11], off
	s_nop 0
	v_addc_co_u32_e32 v21, vcc, 0, v11, vcc
	global_load_dwordx4 v[20:23], v[20:21], off
	s_nop 0
	global_load_dwordx4 v[24:27], v[12:13], off
	v_add_co_u32_e32 v15, vcc, 0x200, v15
	s_xor_b64 s[8:9], vcc, -1
	s_and_b64 s[8:9], exec, s[8:9]
	v_lshl_add_u64 v[12:13], v[12:13], 0, s[6:7]
	v_lshl_add_u64 v[10:11], v[10:11], 0, s[6:7]
	s_or_b64 s[0:1], s[8:9], s[0:1]
	s_waitcnt vmcnt(2)
	ds_write_b128 v14, v[16:19] offset:16384
	s_waitcnt vmcnt(1)
	v_pk_add_f32 v[16:17], v[22:23], 1.0 op_sel_hi:[1,0]
	v_pk_add_f32 v[20:21], v[20:21], 1.0 op_sel_hi:[1,0]
	s_waitcnt vmcnt(0)
	v_pk_mul_f32 v[18:19], v[26:27], v[16:17]
	v_pk_mul_f32 v[16:17], v[24:25], v[20:21]
	ds_write_b128 v14, v[16:19]
	v_add_u32_e32 v14, 0x2000, v14
	s_andn2_b64 exec, exec, s[0:1]
	s_cbranch_execnz .LBB0_2292
	s_or_b64 exec, exec, s[0:1]
	s_lshl_b32 s0, s18, 5
	s_add_i32 s8, s0, s14
	s_ashr_i32 s9, s8, 31
	s_lshl_b64 s[0:1], s[8:9], 13
	v_lshl_add_u64 v[10:11], v[2:3], 0, s[0:1]
	s_waitcnt lgkmcnt(0)
	s_barrier
	global_load_dwordx2 v[12:13], v[10:11], off nt
	global_load_dwordx2 v[14:15], v[10:11], off offset:512 nt
	global_load_dwordx2 v[16:17], v[10:11], off offset:1024 nt
	global_load_dwordx2 v[18:19], v[10:11], off offset:1536 nt
	global_load_dwordx2 v[20:21], v[10:11], off offset:2048 nt
	global_load_dwordx2 v[22:23], v[10:11], off offset:2560 nt
	global_load_dwordx2 v[24:25], v[10:11], off offset:3072 nt
	global_load_dwordx2 v[26:27], v[10:11], off offset:3584 nt
	s_or_b32 s10, s8, 1
	s_ashr_i32 s11, s10, 31
	v_add_co_u32_e32 v10, vcc, s15, v10
	s_lshl_b64 s[0:1], s[10:11], 13
	s_nop 0
	v_addc_co_u32_e32 v11, vcc, 0, v11, vcc
	v_lshl_add_u64 v[42:43], v[2:3], 0, s[0:1]
	v_add_co_u32_e32 v150, vcc, s15, v42
	global_load_dwordx2 v[28:29], v[10:11], off nt
	global_load_dwordx2 v[30:31], v[10:11], off offset:512 nt
	global_load_dwordx2 v[32:33], v[10:11], off offset:1024 nt
	global_load_dwordx2 v[34:35], v[10:11], off offset:1536 nt
	global_load_dwordx2 v[36:37], v[10:11], off offset:2048 nt
	global_load_dwordx2 v[38:39], v[10:11], off offset:2560 nt
	v_addc_co_u32_e32 v151, vcc, 0, v43, vcc
	global_load_dwordx2 v[40:41], v[10:11], off offset:3072 nt
	s_nop 0
	global_load_dwordx2 v[10:11], v[10:11], off offset:3584 nt
	s_nop 0
	global_load_dwordx2 v[44:45], v[42:43], off nt
	global_load_dwordx2 v[46:47], v[42:43], off offset:512 nt
	global_load_dwordx2 v[48:49], v[42:43], off offset:1024 nt
	global_load_dwordx2 v[50:51], v[42:43], off offset:1536 nt
	global_load_dwordx2 v[52:53], v[42:43], off offset:2048 nt
	global_load_dwordx2 v[102:103], v[42:43], off offset:2560 nt
	global_load_dwordx2 v[108:109], v[42:43], off offset:3072 nt
	global_load_dwordx2 v[148:149], v[42:43], off offset:3584 nt
	global_load_dwordx2 v[152:153], v[150:151], off nt
	global_load_dwordx2 v[154:155], v[150:151], off offset:512 nt
	global_load_dwordx2 v[156:157], v[150:151], off offset:1024 nt
	global_load_dwordx2 v[158:159], v[150:151], off offset:1536 nt
	global_load_dwordx2 v[160:161], v[150:151], off offset:2048 nt
	s_lshl_b64 s[12:13], s[8:9], 12
	s_add_i32 s18, s18, s89
	s_waitcnt vmcnt(28)
	v_and_b32_e32 v139, 0xffff0000, v12
	s_waitcnt vmcnt(27)
	v_lshlrev_b32_e32 v134, 16, v14
	v_and_b32_e32 v135, 0xffff0000, v14
	v_lshlrev_b32_e32 v136, 16, v15
	v_and_b32_e32 v137, 0xffff0000, v15
	global_load_dwordx2 v[14:15], v[150:151], off offset:2560 nt
	s_waitcnt vmcnt(23)
	v_lshlrev_b32_e32 v114, 16, v24
	v_and_b32_e32 v115, 0xffff0000, v24
	v_lshlrev_b32_e32 v116, 16, v25
	v_and_b32_e32 v117, 0xffff0000, v25
	global_load_dwordx2 v[24:25], v[150:151], off offset:3072 nt
	v_and_b32_e32 v141, 0xffff0000, v13
	v_lshlrev_b32_e32 v138, 16, v12
	v_lshlrev_b32_e32 v140, 16, v13
	s_waitcnt vmcnt(23)
	v_lshlrev_b32_e32 v110, 16, v26
	v_and_b32_e32 v111, 0xffff0000, v26
	v_lshlrev_b32_e32 v112, 16, v27
	v_and_b32_e32 v113, 0xffff0000, v27
	s_waitcnt vmcnt(20)
	v_lshlrev_b32_e32 v94, 16, v32
	v_and_b32_e32 v95, 0xffff0000, v32
	s_waitcnt vmcnt(15)
	v_lshlrev_b32_e32 v74, 16, v10
	v_and_b32_e32 v75, 0xffff0000, v10
	v_lshlrev_b32_e32 v76, 16, v11
	v_and_b32_e32 v77, 0xffff0000, v11
	global_load_dwordx2 v[26:27], v[150:151], off offset:3584 nt
	v_mul_f32_e32 v32, v141, v141
	v_fmac_f32_e32 v32, v140, v140
	v_lshlrev_b32_e32 v96, 16, v33
	v_and_b32_e32 v97, 0xffff0000, v33
	v_mul_f32_e32 v33, v137, v137
	v_fmac_f32_e32 v33, v136, v136
	v_and_b32_e32 v131, 0xffff0000, v16
	v_and_b32_e32 v133, 0xffff0000, v17
	v_lshlrev_b32_e32 v130, 16, v16
	v_lshlrev_b32_e32 v132, 16, v17
	v_and_b32_e32 v127, 0xffff0000, v18
	v_and_b32_e32 v129, 0xffff0000, v19
	v_lshlrev_b32_e32 v126, 16, v18
	v_lshlrev_b32_e32 v128, 16, v19
	v_and_b32_e32 v123, 0xffff0000, v20
	v_and_b32_e32 v125, 0xffff0000, v21
	v_lshlrev_b32_e32 v122, 16, v20
	v_lshlrev_b32_e32 v124, 16, v21
	v_and_b32_e32 v119, 0xffff0000, v22
	v_and_b32_e32 v121, 0xffff0000, v23
	v_lshlrev_b32_e32 v118, 16, v22
	v_lshlrev_b32_e32 v120, 16, v23
	v_and_b32_e32 v105, 0xffff0000, v28
	v_and_b32_e32 v107, 0xffff0000, v29
	v_lshlrev_b32_e32 v104, 16, v28
	v_lshlrev_b32_e32 v106, 16, v29
	v_and_b32_e32 v99, 0xffff0000, v30
	v_and_b32_e32 v101, 0xffff0000, v31
	v_lshlrev_b32_e32 v98, 16, v30
	v_lshlrev_b32_e32 v100, 16, v31
	v_and_b32_e32 v91, 0xffff0000, v34
	v_and_b32_e32 v93, 0xffff0000, v35
	v_lshlrev_b32_e32 v90, 16, v34
	v_lshlrev_b32_e32 v92, 16, v35
	v_and_b32_e32 v87, 0xffff0000, v36
	v_and_b32_e32 v89, 0xffff0000, v37
	v_lshlrev_b32_e32 v86, 16, v36
	v_lshlrev_b32_e32 v88, 16, v37
	v_and_b32_e32 v83, 0xffff0000, v38
	v_and_b32_e32 v85, 0xffff0000, v39
	v_lshlrev_b32_e32 v82, 16, v38
	v_lshlrev_b32_e32 v84, 16, v39
	v_and_b32_e32 v79, 0xffff0000, v40
	v_and_b32_e32 v81, 0xffff0000, v41
	v_lshlrev_b32_e32 v78, 16, v40
	v_lshlrev_b32_e32 v80, 16, v41
	s_waitcnt vmcnt(12)
	v_lshlrev_b32_e32 v58, 16, v50
	v_and_b32_e32 v59, 0xffff0000, v50
	v_lshlrev_b32_e32 v60, 16, v51
	v_and_b32_e32 v61, 0xffff0000, v51
	s_waitcnt vmcnt(10)
	v_lshlrev_b32_e32 v50, 16, v102
	v_and_b32_e32 v51, 0xffff0000, v102
	v_lshlrev_b32_e32 v54, 16, v52
	v_and_b32_e32 v55, 0xffff0000, v52
	v_lshlrev_b32_e32 v56, 16, v53
	v_and_b32_e32 v57, 0xffff0000, v53
	v_lshlrev_b32_e32 v52, 16, v103
	v_and_b32_e32 v53, 0xffff0000, v103
	v_lshlrev_b32_e32 v66, 16, v46
	v_and_b32_e32 v67, 0xffff0000, v46
	v_lshlrev_b32_e32 v68, 16, v47
	v_and_b32_e32 v69, 0xffff0000, v47
	s_waitcnt vmcnt(9)
	v_lshlrev_b32_e32 v46, 16, v108
	v_and_b32_e32 v47, 0xffff0000, v108
	v_lshlrev_b32_e32 v62, 16, v48
	s_waitcnt vmcnt(1)
	v_lshlrev_b32_e32 v10, 16, v24
	v_and_b32_e32 v11, 0xffff0000, v24
	v_mul_f32_e32 v24, v139, v139
	v_fmac_f32_e32 v24, v138, v138
	v_add_f32_e32 v24, v24, v32
	v_mul_f32_e32 v32, v135, v135
	v_fmac_f32_e32 v32, v134, v134
	v_add_f32_e32 v32, v32, v33
	v_add_f32_e32 v24, v24, v32
	v_mul_f32_e32 v32, v131, v131
	v_mul_f32_e32 v33, v133, v133
	v_fmac_f32_e32 v32, v130, v130
	v_fmac_f32_e32 v33, v132, v132
	v_add_f32_e32 v32, v32, v33
	v_add_f32_e32 v24, v24, v32
	v_mul_f32_e32 v32, v127, v127
	v_mul_f32_e32 v33, v129, v129
	v_fmac_f32_e32 v32, v126, v126
	v_fmac_f32_e32 v33, v128, v128
	v_add_f32_e32 v32, v32, v33
	v_add_f32_e32 v24, v24, v32
	v_mul_f32_e32 v32, v123, v123
	v_mul_f32_e32 v33, v125, v125
	v_fmac_f32_e32 v32, v122, v122
	v_fmac_f32_e32 v33, v124, v124
	v_add_f32_e32 v32, v32, v33
	v_add_f32_e32 v24, v24, v32
	v_mul_f32_e32 v32, v119, v119
	v_mul_f32_e32 v33, v121, v121
	v_fmac_f32_e32 v32, v118, v118
	v_fmac_f32_e32 v33, v120, v120
	v_add_f32_e32 v32, v32, v33
	v_add_f32_e32 v24, v24, v32
	v_mul_f32_e32 v32, v115, v115
	v_mul_f32_e32 v33, v117, v117
	v_fmac_f32_e32 v32, v114, v114
	v_fmac_f32_e32 v33, v116, v116
	v_add_f32_e32 v32, v32, v33
	v_add_f32_e32 v24, v24, v32
	v_mul_f32_e32 v32, v111, v111
	v_mul_f32_e32 v33, v113, v113
	v_fmac_f32_e32 v32, v110, v110
	v_fmac_f32_e32 v33, v112, v112
	v_add_f32_e32 v32, v32, v33
	v_add_f32_e32 v24, v24, v32
	v_mul_f32_e32 v32, v105, v105
	v_mul_f32_e32 v33, v107, v107
	v_fmac_f32_e32 v32, v104, v104
	v_fmac_f32_e32 v33, v106, v106
	v_add_f32_e32 v32, v32, v33
	v_add_f32_e32 v24, v24, v32
	v_mul_f32_e32 v32, v99, v99
	v_mul_f32_e32 v33, v101, v101
	v_fmac_f32_e32 v32, v98, v98
	v_fmac_f32_e32 v33, v100, v100
	v_add_f32_e32 v32, v32, v33
	v_add_f32_e32 v24, v24, v32
	v_mul_f32_e32 v32, v95, v95
	v_mul_f32_e32 v33, v97, v97
	v_fmac_f32_e32 v32, v94, v94
	v_fmac_f32_e32 v33, v96, v96
	v_add_f32_e32 v32, v32, v33
	v_add_f32_e32 v24, v24, v32
	v_mul_f32_e32 v32, v91, v91
	v_mul_f32_e32 v33, v93, v93
	v_fmac_f32_e32 v32, v90, v90
	v_fmac_f32_e32 v33, v92, v92
	v_add_f32_e32 v32, v32, v33
	v_add_f32_e32 v24, v24, v32
	v_mul_f32_e32 v32, v87, v87
	v_mul_f32_e32 v33, v89, v89
	v_fmac_f32_e32 v32, v86, v86
	v_fmac_f32_e32 v33, v88, v88
	v_add_f32_e32 v32, v32, v33
	v_add_f32_e32 v24, v24, v32
	v_mul_f32_e32 v32, v83, v83
	v_mul_f32_e32 v33, v85, v85
	v_fmac_f32_e32 v32, v82, v82
	v_fmac_f32_e32 v33, v84, v84
	v_add_f32_e32 v32, v32, v33
	v_add_f32_e32 v24, v24, v32
	v_mul_f32_e32 v32, v79, v79
	v_mul_f32_e32 v33, v81, v81
	v_fmac_f32_e32 v32, v78, v78
	v_fmac_f32_e32 v33, v80, v80
	v_add_f32_e32 v32, v32, v33
	v_add_f32_e32 v24, v24, v32
	v_mul_f32_e32 v32, v75, v75
	v_mul_f32_e32 v33, v77, v77
	v_fmac_f32_e32 v32, v74, v74
	v_fmac_f32_e32 v33, v76, v76
	v_add_f32_e32 v32, v32, v33
	v_add_f32_e32 v24, v24, v32
	v_and_b32_e32 v33, 0xffff0000, v25
	v_and_b32_e32 v63, 0xffff0000, v48
	v_add_f32_dpp v24, v24, v24 quad_perm:[1,0,3,2] row_mask:0xf bank_mask:0xf bound_ctrl:1
	v_lshlrev_b32_e32 v64, 16, v49
	v_and_b32_e32 v65, 0xffff0000, v49
	v_add_f32_dpp v24, v24, v24 quad_perm:[2,3,0,1] row_mask:0xf bank_mask:0xf bound_ctrl:1
	v_lshlrev_b32_e32 v48, 16, v109
	v_and_b32_e32 v49, 0xffff0000, v109
	v_add_f32_dpp v24, v24, v24 row_half_mirror row_mask:0xf bank_mask:0xf bound_ctrl:1
	v_lshlrev_b32_e32 v42, 16, v148
	v_and_b32_e32 v43, 0xffff0000, v148
	v_add_f32_dpp v24, v24, v24 row_mirror row_mask:0xf bank_mask:0xf bound_ctrl:1
	v_mov_b32_e32 v32, v24
	s_nop 1
	v_permlane16_swap_b32 v24, v32
	v_lshlrev_b32_e32 v70, 16, v44
	v_add_f32_e32 v24, v24, v32
	v_mov_b32_e32 v32, v24
	s_nop 1
	v_permlane32_swap_b32 v24, v32
	v_and_b32_e32 v71, 0xffff0000, v44
	v_add_f32_e32 v24, v24, v32
	v_fmamk_f32 v24, v24, 0x39800000, v145
	v_mul_f32_e32 v32, 0x4f800000, v24
	v_cmp_gt_f32_e32 vcc, s16, v24
	v_lshlrev_b32_e32 v72, 16, v45
	v_and_b32_e32 v73, 0xffff0000, v45
	v_cndmask_b32_e32 v102, v24, v32, vcc
	v_sqrt_f32_e32 v103, v102
	v_lshlrev_b32_e32 v32, 16, v25
	v_lshlrev_b32_e32 v44, 16, v149
	v_and_b32_e32 v45, 0xffff0000, v149
	v_add_u32_e32 v25, -1, v103
	v_fma_f32 v108, -v25, v103, v102
	v_cmp_ge_f32_e64 s[0:1], 0, v108
	v_add_u32_e32 v108, 1, v103
	v_lshlrev_b32_e32 v38, 16, v152
	v_cndmask_b32_e64 v25, v103, v25, s[0:1]
	v_fma_f32 v103, -v108, v103, v102
	v_cmp_lt_f32_e64 s[0:1], 0, v103
	v_and_b32_e32 v39, 0xffff0000, v152
	v_lshlrev_b32_e32 v40, 16, v153
	v_cndmask_b32_e64 v25, v25, v108, s[0:1]
	v_mul_f32_e32 v103, 0x37800000, v25
	v_cndmask_b32_e32 v25, v25, v103, vcc
	v_cmp_class_f32_e32 vcc, v102, v146
	v_and_b32_e32 v41, 0xffff0000, v153
	v_lshlrev_b32_e32 v34, 16, v154
	v_cndmask_b32_e32 v102, v25, v102, vcc
	v_div_scale_f32 v103, s[0:1], v102, v102, 1.0
	v_rcp_f32_e32 v108, v103
	v_and_b32_e32 v35, 0xffff0000, v154
	v_lshlrev_b32_e32 v36, 16, v155
	v_and_b32_e32 v37, 0xffff0000, v155
	v_fma_f32 v109, -v103, v108, 1.0
	v_fmac_f32_e32 v108, v109, v108
	v_div_scale_f32 v109, vcc, 1.0, v102, 1.0
	v_mul_f32_e32 v148, v109, v108
	v_fma_f32 v149, -v103, v148, v109
	v_fmac_f32_e32 v148, v149, v108
	v_fma_f32 v103, -v103, v148, v109
	v_div_fmas_f32 v103, v103, v108, v148
	ds_read_b128 v[148:151], v1
	ds_read_b128 v[152:155], v1 offset:16384
	v_div_fixup_f32 v108, v103, v102, 1.0
	v_lshlrev_b32_e32 v16, 16, v160
	v_and_b32_e32 v17, 0xffff0000, v160
	v_lshlrev_b32_e32 v18, 16, v161
	v_and_b32_e32 v19, 0xffff0000, v161
	v_pk_mul_f32 v[160:161], v[108:109], v[138:139] op_sel_hi:[0,1]
	s_waitcnt lgkmcnt(0)
	v_pk_fma_f32 v[148:149], v[148:149], v[160:161], v[152:153]
	v_lshlrev_b32_e32 v28, 16, v156
	v_and_b32_e32 v29, 0xffff0000, v156
	v_lshlrev_b32_e32 v30, 16, v157
	v_and_b32_e32 v31, 0xffff0000, v157
	v_lshlrev_b32_e32 v20, 16, v158
	v_and_b32_e32 v21, 0xffff0000, v158
	v_lshlrev_b32_e32 v22, 16, v159
	v_and_b32_e32 v23, 0xffff0000, v159
	v_pk_mul_f32 v[162:163], v[108:109], v[140:141] op_sel_hi:[0,1]
	ds_read_b128 v[138:141], v1 offset:1024
	ds_read_b128 v[156:159], v1 offset:17408
	v_mul_f32_e32 v109, 0x41800000, v148
	v_mul_f32_e32 v148, 0x41800000, v149
	v_pk_fma_f32 v[150:151], v[150:151], v[162:163], v[154:155]
	v_med3_f32 v109, v109, s17, v147
	v_med3_f32 v148, v148, s17, v147
	v_mov_b32_e32 v160, 0
	v_cvt_pk_fp8_f32 v160, v109, v148
	v_mul_f32_e32 v109, 0x41800000, v151
	v_med3_f32 v109, v109, s17, v147
	v_mul_f32_e32 v149, 0x41800000, v150
	v_pk_mul_f32 v[134:135], v[108:109], v[134:135] op_sel_hi:[0,1]
	v_med3_f32 v148, v149, s17, v147
	s_waitcnt lgkmcnt(0)
	v_pk_fma_f32 v[134:135], v[138:139], v[134:135], v[156:157]
	v_cvt_pk_fp8_f32 v160, v148, v109 op_sel:[0,0,1]
	v_pk_mul_f32 v[136:137], v[108:109], v[136:137] op_sel_hi:[0,1]
	v_mul_f32_e32 v109, 0x41800000, v134
	v_mul_f32_e32 v134, 0x41800000, v135
	v_med3_f32 v109, v109, s17, v147
	v_med3_f32 v134, v134, s17, v147
	v_mov_b32_e32 v156, 0
	v_cvt_pk_fp8_f32 v156, v109, v134
	v_pk_fma_f32 v[136:137], v[140:141], v[136:137], v[158:159]
	v_lshl_add_u64 v[102:103], v[4:5], 0, s[12:13]
	v_mul_f32_e32 v135, 0x41800000, v136
	v_mul_f32_e32 v109, 0x41800000, v137
	v_med3_f32 v134, v135, s17, v147
	v_med3_f32 v109, v109, s17, v147
	v_cvt_pk_fp8_f32 v156, v134, v109 op_sel:[0,0,1]
	ds_read_b128 v[134:137], v1 offset:2048
	ds_read_b128 v[138:141], v1 offset:18432
	v_pk_mul_f32 v[152:153], v[108:109], v[130:131] op_sel_hi:[0,1]
	v_pk_mul_f32 v[154:155], v[108:109], v[132:133] op_sel_hi:[0,1]
	ds_read_b128 v[130:133], v1 offset:3072
	ds_read_b128 v[148:151], v1 offset:19456
	s_or_b32 s0, s8, 2
	s_waitcnt lgkmcnt(2)
	v_pk_fma_f32 v[134:135], v[152:153], v[134:135], v[138:139]
	v_pk_fma_f32 v[136:137], v[154:155], v[136:137], v[140:141]
	v_mul_f32_e32 v109, 0x41800000, v134
	v_mul_f32_e32 v134, 0x41800000, v135
	v_mul_f32_e32 v135, 0x41800000, v136
	v_med3_f32 v109, v109, s17, v147
	v_med3_f32 v134, v134, s17, v147
	v_mov_b32_e32 v136, 0
	v_cvt_pk_fp8_f32 v136, v109, v134
	v_mul_f32_e32 v109, 0x41800000, v137
	v_med3_f32 v109, v109, s17, v147
	v_pk_mul_f32 v[126:127], v[108:109], v[126:127] op_sel_hi:[0,1]
	v_med3_f32 v134, v135, s17, v147
	v_pk_mul_f32 v[128:129], v[108:109], v[128:129] op_sel_hi:[0,1]
	s_waitcnt lgkmcnt(0)
	v_pk_fma_f32 v[126:127], v[126:127], v[130:131], v[148:149]
	v_cvt_pk_fp8_f32 v136, v134, v109 op_sel:[0,0,1]
	v_pk_fma_f32 v[128:129], v[128:129], v[132:133], v[150:151]
	v_mul_f32_e32 v109, 0x41800000, v126
	v_mul_f32_e32 v126, 0x41800000, v127
	v_mul_f32_e32 v127, 0x41800000, v128
	v_med3_f32 v109, v109, s17, v147
	v_med3_f32 v126, v126, s17, v147
	v_mov_b32_e32 v128, 0
	v_cvt_pk_fp8_f32 v128, v109, v126
	v_mul_f32_e32 v109, 0x41800000, v129
	v_med3_f32 v126, v127, s17, v147
	v_med3_f32 v109, v109, s17, v147
	v_cvt_pk_fp8_f32 v128, v126, v109 op_sel:[0,0,1]
	global_store_dword v[102:103], v160, off
	global_store_dword v[102:103], v156, off offset:256
	global_store_dword v[102:103], v136, off offset:512
	global_store_dword v[102:103], v128, off offset:768
	ds_read_b128 v[126:129], v1 offset:4096
	ds_read_b128 v[130:133], v1 offset:20480
	v_pk_mul_f32 v[138:139], v[108:109], v[122:123] op_sel_hi:[0,1]
	v_pk_mul_f32 v[140:141], v[108:109], v[124:125] op_sel_hi:[0,1]
	ds_read_b128 v[122:125], v1 offset:5120
	ds_read_b128 v[134:137], v1 offset:21504
	s_ashr_i32 s1, s0, 31
	s_waitcnt lgkmcnt(2)
	v_pk_fma_f32 v[126:127], v[138:139], v[126:127], v[130:131]
	v_pk_fma_f32 v[128:129], v[140:141], v[128:129], v[132:133]
	v_mul_f32_e32 v109, 0x41800000, v126
	v_mul_f32_e32 v126, 0x41800000, v127
	v_med3_f32 v109, v109, s17, v147
	v_med3_f32 v126, v126, s17, v147
	v_mov_b32_e32 v138, 0
	v_cvt_pk_fp8_f32 v138, v109, v126
	v_mul_f32_e32 v109, 0x41800000, v129
	v_med3_f32 v109, v109, s17, v147
	v_mul_f32_e32 v127, 0x41800000, v128
	v_pk_mul_f32 v[118:119], v[108:109], v[118:119] op_sel_hi:[0,1]
	v_med3_f32 v126, v127, s17, v147
	s_waitcnt lgkmcnt(0)
	v_pk_fma_f32 v[118:119], v[118:119], v[122:123], v[134:135]
	v_cvt_pk_fp8_f32 v138, v126, v109 op_sel:[0,0,1]
	v_pk_mul_f32 v[120:121], v[108:109], v[120:121] op_sel_hi:[0,1]
	v_mul_f32_e32 v109, 0x41800000, v118
	v_mul_f32_e32 v118, 0x41800000, v119
	v_med3_f32 v109, v109, s17, v147
	v_med3_f32 v118, v118, s17, v147
	v_mov_b32_e32 v134, 0
	v_cvt_pk_fp8_f32 v134, v109, v118
	v_pk_fma_f32 v[120:121], v[120:121], v[124:125], v[136:137]
	s_lshl_b64 s[12:13], s[0:1], 13
	v_mul_f32_e32 v119, 0x41800000, v120
	v_mul_f32_e32 v109, 0x41800000, v121
	v_med3_f32 v118, v119, s17, v147
	v_med3_f32 v109, v109, s17, v147
	v_cvt_pk_fp8_f32 v134, v118, v109 op_sel:[0,0,1]
	ds_read_b128 v[118:121], v1 offset:6144
	ds_read_b128 v[122:125], v1 offset:22528
	v_pk_mul_f32 v[130:131], v[108:109], v[114:115] op_sel_hi:[0,1]
	v_pk_mul_f32 v[132:133], v[108:109], v[116:117] op_sel_hi:[0,1]
	ds_read_b128 v[114:117], v1 offset:7168
	ds_read_b128 v[126:129], v1 offset:23552
	v_lshlrev_b32_e32 v12, 16, v14
	s_waitcnt lgkmcnt(2)
	v_pk_fma_f32 v[118:119], v[130:131], v[118:119], v[122:123]
	v_pk_fma_f32 v[120:121], v[132:133], v[120:121], v[124:125]
	v_mul_f32_e32 v109, 0x41800000, v118
	v_mul_f32_e32 v118, 0x41800000, v119
	v_mul_f32_e32 v119, 0x41800000, v120
	v_med3_f32 v109, v109, s17, v147
	v_med3_f32 v118, v118, s17, v147
	v_mov_b32_e32 v120, 0
	v_cvt_pk_fp8_f32 v120, v109, v118
	v_mul_f32_e32 v109, 0x41800000, v121
	v_med3_f32 v109, v109, s17, v147
	v_pk_mul_f32 v[110:111], v[108:109], v[110:111] op_sel_hi:[0,1]
	v_med3_f32 v118, v119, s17, v147
	v_pk_mul_f32 v[112:113], v[108:109], v[112:113] op_sel_hi:[0,1]
	s_waitcnt lgkmcnt(0)
	v_pk_fma_f32 v[110:111], v[110:111], v[114:115], v[126:127]
	v_cvt_pk_fp8_f32 v120, v118, v109 op_sel:[0,0,1]
	v_pk_fma_f32 v[112:113], v[112:113], v[116:117], v[128:129]
	v_mul_f32_e32 v109, 0x41800000, v110
	v_mul_f32_e32 v110, 0x41800000, v111
	v_mul_f32_e32 v111, 0x41800000, v112
	v_med3_f32 v109, v109, s17, v147
	v_med3_f32 v110, v110, s17, v147
	v_mov_b32_e32 v112, 0
	v_cvt_pk_fp8_f32 v112, v109, v110
	v_mul_f32_e32 v109, 0x41800000, v113
	v_med3_f32 v110, v111, s17, v147
	v_med3_f32 v109, v109, s17, v147
	v_cvt_pk_fp8_f32 v112, v110, v109 op_sel:[0,0,1]
	global_store_dword v[102:103], v138, off offset:1024
	global_store_dword v[102:103], v134, off offset:1280
	global_store_dword v[102:103], v120, off offset:1536
	global_store_dword v[102:103], v112, off offset:1792
	ds_read_b128 v[110:113], v1 offset:8192
	ds_read_b128 v[114:117], v1 offset:24576
	v_pk_mul_f32 v[122:123], v[108:109], v[104:105] op_sel_hi:[0,1]
	v_pk_mul_f32 v[124:125], v[108:109], v[106:107] op_sel_hi:[0,1]
	ds_read_b128 v[104:107], v1 offset:9216
	ds_read_b128 v[118:121], v1 offset:25600
	v_and_b32_e32 v13, 0xffff0000, v14
	s_waitcnt lgkmcnt(2)
	v_pk_fma_f32 v[110:111], v[122:123], v[110:111], v[114:115]
	v_pk_fma_f32 v[112:113], v[124:125], v[112:113], v[116:117]
	v_mul_f32_e32 v109, 0x41800000, v110
	v_mul_f32_e32 v110, 0x41800000, v111
	v_med3_f32 v109, v109, s17, v147
	v_med3_f32 v110, v110, s17, v147
	v_mov_b32_e32 v122, 0
	v_cvt_pk_fp8_f32 v122, v109, v110
	v_mul_f32_e32 v109, 0x41800000, v113
	v_med3_f32 v109, v109, s17, v147
	v_pk_mul_f32 v[98:99], v[108:109], v[98:99] op_sel_hi:[0,1]
	v_mul_f32_e32 v111, 0x41800000, v112
	s_waitcnt lgkmcnt(0)
	v_pk_fma_f32 v[98:99], v[98:99], v[104:105], v[118:119]
	v_med3_f32 v110, v111, s17, v147
	v_mul_f32_e32 v98, 0x41800000, v98
	v_mul_f32_e32 v99, 0x41800000, v99
	v_cvt_pk_fp8_f32 v122, v110, v109 op_sel:[0,0,1]
	v_pk_mul_f32 v[100:101], v[108:109], v[100:101] op_sel_hi:[0,1]
	v_med3_f32 v98, v98, s17, v147
	v_med3_f32 v99, v99, s17, v147
	v_mov_b32_e32 v109, 0
	v_cvt_pk_fp8_f32 v109, v98, v99
	v_pk_fma_f32 v[100:101], v[100:101], v[106:107], v[120:121]
	v_lshlrev_b32_e32 v14, 16, v15
	v_mul_f32_e32 v100, 0x41800000, v100
	v_mul_f32_e32 v98, 0x41800000, v101
	v_med3_f32 v99, v100, s17, v147
	v_med3_f32 v98, v98, s17, v147
	v_cvt_pk_fp8_f32 v109, v99, v98 op_sel:[0,0,1]
	ds_read_b128 v[98:101], v1 offset:10240
	ds_read_b128 v[104:107], v1 offset:26624
	v_and_b32_e32 v15, 0xffff0000, v15
	s_waitcnt vmcnt(8)
	v_lshlrev_b32_e32 v24, 16, v26
	v_pk_mul_f32 v[114:115], v[108:109], v[94:95] op_sel_hi:[0,1]
	v_pk_mul_f32 v[116:117], v[108:109], v[96:97] op_sel_hi:[0,1]
	ds_read_b128 v[94:97], v1 offset:11264
	ds_read_b128 v[110:113], v1 offset:27648
	s_waitcnt lgkmcnt(2)
	v_pk_fma_f32 v[98:99], v[114:115], v[98:99], v[104:105]
	v_pk_mul_f32 v[90:91], v[108:109], v[90:91] op_sel_hi:[0,1]
	v_mul_f32_e32 v98, 0x41800000, v98
	v_mul_f32_e32 v99, 0x41800000, v99
	s_waitcnt lgkmcnt(0)
	v_pk_fma_f32 v[90:91], v[90:91], v[94:95], v[110:111]
	v_med3_f32 v98, v98, s17, v147
	v_med3_f32 v99, v99, s17, v147
	v_mov_b32_e32 v104, 0
	v_mul_f32_e32 v90, 0x41800000, v90
	v_mul_f32_e32 v91, 0x41800000, v91
	v_cvt_pk_fp8_f32 v104, v98, v99
	v_med3_f32 v90, v90, s17, v147
	v_med3_f32 v91, v91, s17, v147
	v_mov_b32_e32 v94, 0
	v_pk_fma_f32 v[100:101], v[116:117], v[100:101], v[106:107]
	v_pk_mul_f32 v[92:93], v[108:109], v[92:93] op_sel_hi:[0,1]
	v_cvt_pk_fp8_f32 v94, v90, v91
	v_mul_f32_e32 v100, 0x41800000, v100
	v_mul_f32_e32 v98, 0x41800000, v101
	v_pk_fma_f32 v[92:93], v[92:93], v[96:97], v[112:113]
	v_med3_f32 v99, v100, s17, v147
	v_med3_f32 v98, v98, s17, v147
	v_mul_f32_e32 v92, 0x41800000, v92
	v_mul_f32_e32 v90, 0x41800000, v93
	v_cvt_pk_fp8_f32 v104, v99, v98 op_sel:[0,0,1]
	v_med3_f32 v91, v92, s17, v147
	v_med3_f32 v90, v90, s17, v147
	v_cvt_pk_fp8_f32 v94, v91, v90 op_sel:[0,0,1]
	global_store_dword v[102:103], v122, off offset:2048
	global_store_dword v[102:103], v109, off offset:2304
	global_store_dword v[102:103], v104, off offset:2560
	global_store_dword v[102:103], v94, off offset:2816
	ds_read_b128 v[90:93], v1 offset:12288
	ds_read_b128 v[94:97], v1 offset:28672
	v_pk_mul_f32 v[104:105], v[108:109], v[86:87] op_sel_hi:[0,1]
	v_pk_mul_f32 v[106:107], v[108:109], v[88:89] op_sel_hi:[0,1]
	ds_read_b128 v[86:89], v1 offset:13312
	ds_read_b128 v[98:101], v1 offset:14336
	v_pk_mul_f32 v[78:79], v[108:109], v[78:79] op_sel_hi:[0,1]
	s_waitcnt lgkmcnt(2)
	v_pk_fma_f32 v[90:91], v[104:105], v[90:91], v[94:95]
	v_pk_fma_f32 v[92:93], v[106:107], v[92:93], v[96:97]
	v_mul_f32_e32 v90, 0x41800000, v90
	v_mul_f32_e32 v91, 0x41800000, v91
	v_mul_f32_e32 v92, 0x41800000, v92
	v_mul_f32_e32 v93, 0x41800000, v93
	v_med3_f32 v90, v90, s17, v147
	v_med3_f32 v91, v91, s17, v147
	v_mov_b32_e32 v104, 0
	v_cvt_pk_fp8_f32 v104, v90, v91
	v_med3_f32 v94, v92, s17, v147
	v_med3_f32 v95, v93, s17, v147
	ds_read_b128 v[90:93], v1 offset:29696
	v_cvt_pk_fp8_f32 v104, v94, v95 op_sel:[0,0,1]
	v_pk_mul_f32 v[94:95], v[108:109], v[82:83] op_sel_hi:[0,1]
	v_pk_mul_f32 v[96:97], v[108:109], v[84:85] op_sel_hi:[0,1]
	ds_read_b128 v[82:85], v1 offset:30720
	s_waitcnt lgkmcnt(1)
	v_pk_fma_f32 v[86:87], v[94:95], v[86:87], v[90:91]
	v_mov_b32_e32 v90, 0
	v_mul_f32_e32 v86, 0x41800000, v86
	v_mul_f32_e32 v87, 0x41800000, v87
	v_med3_f32 v86, v86, s17, v147
	v_med3_f32 v87, v87, s17, v147
	v_cvt_pk_fp8_f32 v90, v86, v87
	v_pk_fma_f32 v[88:89], v[96:97], v[88:89], v[92:93]
	v_pk_mul_f32 v[80:81], v[108:109], v[80:81] op_sel_hi:[0,1]
	v_mul_f32_e32 v88, 0x41800000, v88
	v_mul_f32_e32 v86, 0x41800000, v89
	s_waitcnt lgkmcnt(0)
;     ...
;         NR_LOAD(va, m0); NR_LOAD(vb, m0 + 1); NR_FIN(va, m0); NR_LOAD(va, m0 + 2); NR_FIN(vb, m0 + 1); NR_LOAD(vb, m0 + 3); NR_FIN(va, m0 + 2); NR_FIN(vb, m0 + 3);
	v_pk_fma_f32 v[78:79], v[78:79], v[98:99], v[82:83]
	v_med3_f32 v87, v88, s17, v147
	v_med3_f32 v86, v86, s17, v147
	v_pk_fma_f32 v[80:81], v[80:81], v[100:101], v[84:85]
	v_mul_f32_e32 v78, 0x41800000, v78
	v_mul_f32_e32 v79, 0x41800000, v79
	v_cvt_pk_fp8_f32 v90, v87, v86 op_sel:[0,0,1]
	v_mul_f32_e32 v80, 0x41800000, v80
	v_med3_f32 v78, v78, s17, v147
	v_med3_f32 v79, v79, s17, v147
	v_mov_b32_e32 v87, 0
	v_mul_f32_e32 v86, 0x41800000, v81
	v_cvt_pk_fp8_f32 v87, v78, v79
	v_med3_f32 v88, v80, s17, v147
	ds_read_b128 v[78:81], v142
	ds_read_b128 v[82:85], v142 offset:16384
	v_pk_mul_f32 v[74:75], v[108:109], v[74:75] op_sel_hi:[0,1]
	v_pk_mul_f32 v[76:77], v[108:109], v[76:77] op_sel_hi:[0,1]
	v_med3_f32 v86, v86, s17, v147
	v_cvt_pk_fp8_f32 v87, v88, v86 op_sel:[0,0,1]
	s_waitcnt lgkmcnt(0)
	v_pk_fma_f32 v[74:75], v[74:75], v[78:79], v[82:83]
	v_mov_b32_e32 v78, 0
	v_mul_f32_e32 v74, 0x41800000, v74
	v_mul_f32_e32 v75, 0x41800000, v75
	v_med3_f32 v74, v74, s17, v147
	v_med3_f32 v75, v75, s17, v147
	v_cvt_pk_fp8_f32 v78, v74, v75
	v_pk_fma_f32 v[76:77], v[76:77], v[80:81], v[84:85]
	v_mul_f32_e32 v108, v69, v69
	v_mul_f32_e32 v76, 0x41800000, v76
	v_mul_f32_e32 v74, 0x41800000, v77
	v_med3_f32 v75, v76, s17, v147
	v_med3_f32 v74, v74, s17, v147
	v_cvt_pk_fp8_f32 v78, v75, v74 op_sel:[0,0,1]
	global_store_dword v[102:103], v104, off offset:3072
	global_store_dword v[102:103], v90, off offset:3328
	global_store_dword v[102:103], v87, off offset:3584
	global_store_dword v[102:103], v78, off offset:3840
	v_lshl_add_u64 v[74:75], v[2:3], 0, s[12:13]
	global_load_dwordx2 v[76:77], v[74:75], off nt
	global_load_dwordx2 v[106:107], v[74:75], off offset:512 nt
	global_load_dwordx2 v[104:105], v[74:75], off offset:1024 nt
	global_load_dwordx2 v[102:103], v[74:75], off offset:1536 nt
	global_load_dwordx2 v[100:101], v[74:75], off offset:2048 nt
	global_load_dwordx2 v[98:99], v[74:75], off offset:2560 nt
	global_load_dwordx2 v[96:97], v[74:75], off offset:3072 nt
	global_load_dwordx2 v[92:93], v[74:75], off offset:3584 nt
	v_add_co_u32_e32 v74, vcc, s15, v74
	v_fmac_f32_e32 v108, v68, v68
	s_nop 0
	v_addc_co_u32_e32 v75, vcc, 0, v75, vcc
	global_load_dwordx2 v[94:95], v[74:75], off nt
	global_load_dwordx2 v[86:87], v[74:75], off offset:512 nt
	global_load_dwordx2 v[78:79], v[74:75], off offset:1024 nt
	global_load_dwordx2 v[80:81], v[74:75], off offset:1536 nt
	global_load_dwordx2 v[82:83], v[74:75], off offset:2048 nt
	global_load_dwordx2 v[84:85], v[74:75], off offset:2560 nt
	global_load_dwordx2 v[88:89], v[74:75], off offset:3072 nt
	global_load_dwordx2 v[90:91], v[74:75], off offset:3584 nt
	v_mul_f32_e32 v74, v71, v71
	v_mul_f32_e32 v75, v73, v73
	v_fmac_f32_e32 v74, v70, v70
	v_fmac_f32_e32 v75, v72, v72
	v_add_f32_e32 v74, v74, v75
	v_mul_f32_e32 v75, v67, v67
	v_fmac_f32_e32 v75, v66, v66
	v_add_f32_e32 v75, v75, v108
	v_add_f32_e32 v74, v74, v75
	v_mul_f32_e32 v75, v63, v63
	v_mul_f32_e32 v108, v65, v65
	v_fmac_f32_e32 v75, v62, v62
	v_fmac_f32_e32 v108, v64, v64
	v_add_f32_e32 v75, v75, v108
	v_add_f32_e32 v74, v74, v75
	v_mul_f32_e32 v75, v59, v59
	v_mul_f32_e32 v108, v61, v61
	v_fmac_f32_e32 v75, v58, v58
	v_fmac_f32_e32 v108, v60, v60
	v_add_f32_e32 v75, v75, v108
	v_add_f32_e32 v74, v74, v75
	v_mul_f32_e32 v75, v55, v55
	v_mul_f32_e32 v108, v57, v57
	v_fmac_f32_e32 v75, v54, v54
	v_fmac_f32_e32 v108, v56, v56
	v_add_f32_e32 v75, v75, v108
	v_add_f32_e32 v74, v74, v75
	v_mul_f32_e32 v75, v51, v51
	v_mul_f32_e32 v108, v53, v53
	v_fmac_f32_e32 v75, v50, v50
	v_fmac_f32_e32 v108, v52, v52
	v_add_f32_e32 v75, v75, v108
	v_add_f32_e32 v74, v74, v75
	v_mul_f32_e32 v75, v47, v47
	v_mul_f32_e32 v108, v49, v49
	v_fmac_f32_e32 v75, v46, v46
	v_fmac_f32_e32 v108, v48, v48
	v_add_f32_e32 v75, v75, v108
	v_add_f32_e32 v74, v74, v75
	v_mul_f32_e32 v75, v43, v43
	v_mul_f32_e32 v108, v45, v45
	v_fmac_f32_e32 v75, v42, v42
	v_fmac_f32_e32 v108, v44, v44
	v_add_f32_e32 v75, v75, v108
	v_add_f32_e32 v74, v74, v75
	v_mul_f32_e32 v75, v39, v39
	v_mul_f32_e32 v108, v41, v41
	v_fmac_f32_e32 v75, v38, v38
	v_fmac_f32_e32 v108, v40, v40
	v_add_f32_e32 v75, v75, v108
	v_add_f32_e32 v74, v74, v75
	v_mul_f32_e32 v75, v35, v35
	v_mul_f32_e32 v108, v37, v37
	v_fmac_f32_e32 v75, v34, v34
	v_fmac_f32_e32 v108, v36, v36
	v_add_f32_e32 v75, v75, v108
	v_add_f32_e32 v74, v74, v75
	v_mul_f32_e32 v75, v29, v29
	v_mul_f32_e32 v108, v31, v31
	v_fmac_f32_e32 v75, v28, v28
	v_fmac_f32_e32 v108, v30, v30
	v_add_f32_e32 v75, v75, v108
	v_add_f32_e32 v74, v74, v75
	v_mul_f32_e32 v75, v21, v21
	v_mul_f32_e32 v108, v23, v23
	v_fmac_f32_e32 v75, v20, v20
	v_fmac_f32_e32 v108, v22, v22
	v_add_f32_e32 v75, v75, v108
	v_add_f32_e32 v74, v74, v75
	v_mul_f32_e32 v75, v17, v17
	v_mul_f32_e32 v108, v19, v19
	v_fmac_f32_e32 v75, v16, v16
	v_fmac_f32_e32 v108, v18, v18
	v_add_f32_e32 v75, v75, v108
	v_add_f32_e32 v74, v74, v75
	v_mul_f32_e32 v75, v13, v13
	v_mul_f32_e32 v108, v15, v15
	v_fmac_f32_e32 v75, v12, v12
	v_fmac_f32_e32 v108, v14, v14
	v_add_f32_e32 v75, v75, v108
	v_add_f32_e32 v74, v74, v75
	v_mul_f32_e32 v75, v11, v11
	v_mul_f32_e32 v108, v33, v33
	v_fmac_f32_e32 v75, v10, v10
	v_fmac_f32_e32 v108, v32, v32
	v_and_b32_e32 v25, 0xffff0000, v26
	v_lshlrev_b32_e32 v26, 16, v27
	v_and_b32_e32 v27, 0xffff0000, v27
	v_add_f32_e32 v75, v75, v108
	v_add_f32_e32 v74, v74, v75
	v_mul_f32_e32 v75, v25, v25
	v_mul_f32_e32 v108, v27, v27
	v_fmac_f32_e32 v75, v24, v24
	v_fmac_f32_e32 v108, v26, v26
	v_add_f32_e32 v75, v75, v108
	v_add_f32_e32 v74, v74, v75
	s_lshl_b64 s[12:13], s[10:11], 12
	s_lshl_b64 s[10:11], s[0:1], 12
	v_add_f32_dpp v74, v74, v74 quad_perm:[1,0,3,2] row_mask:0xf bank_mask:0xf bound_ctrl:1
	s_or_b32 s8, s8, 3
	s_ashr_i32 s9, s8, 31
	v_add_f32_dpp v74, v74, v74 quad_perm:[2,3,0,1] row_mask:0xf bank_mask:0xf bound_ctrl:1
	s_waitcnt vmcnt(14)
	v_and_b32_e32 v139, 0xffff0000, v106
	v_and_b32_e32 v141, 0xffff0000, v107
	v_add_f32_dpp v74, v74, v74 row_half_mirror row_mask:0xf bank_mask:0xf bound_ctrl:1
	v_lshlrev_b32_e32 v138, 16, v106
	v_lshlrev_b32_e32 v140, 16, v107
	v_add_f32_dpp v74, v74, v74 row_mirror row_mask:0xf bank_mask:0xf bound_ctrl:1
	v_mov_b32_e32 v75, v74
	s_nop 1
	v_permlane16_swap_b32 v74, v75
	s_waitcnt vmcnt(13)
	v_and_b32_e32 v135, 0xffff0000, v104
	v_add_f32_e32 v74, v74, v75
	v_mov_b32_e32 v75, v74
	s_nop 1
	v_permlane32_swap_b32 v74, v75
	v_and_b32_e32 v137, 0xffff0000, v105
	v_add_f32_e32 v74, v74, v75
	v_fmamk_f32 v74, v74, 0x39800000, v145
	v_mul_f32_e32 v75, 0x4f800000, v74
	v_cmp_gt_f32_e32 vcc, s16, v74
	v_lshlrev_b32_e32 v134, 16, v104
	v_lshlrev_b32_e32 v136, 16, v105
	v_cndmask_b32_e32 v74, v74, v75, vcc
	v_sqrt_f32_e32 v75, v74
	s_waitcnt vmcnt(12)
	v_and_b32_e32 v131, 0xffff0000, v102
	v_and_b32_e32 v133, 0xffff0000, v103
	v_lshlrev_b32_e32 v130, 16, v102
	v_add_u32_e32 v108, -1, v75
	v_fma_f32 v109, -v108, v75, v74
	v_cmp_ge_f32_e64 s[0:1], 0, v109
	v_add_u32_e32 v109, 1, v75
	v_lshlrev_b32_e32 v132, 16, v103
	v_cndmask_b32_e64 v108, v75, v108, s[0:1]
	v_fma_f32 v75, -v109, v75, v74
	v_cmp_lt_f32_e64 s[0:1], 0, v75
	s_waitcnt vmcnt(11)
	v_and_b32_e32 v129, 0xffff0000, v101
	v_lshlrev_b32_e32 v128, 16, v101
	v_cndmask_b32_e64 v75, v108, v109, s[0:1]
	v_mul_f32_e32 v108, 0x37800000, v75
	v_cndmask_b32_e32 v75, v75, v108, vcc
	v_cmp_class_f32_e32 vcc, v74, v146
	s_waitcnt vmcnt(6)
	v_and_b32_e32 v107, 0xffff0000, v86
	v_lshlrev_b32_e32 v106, 16, v86
	v_cndmask_b32_e32 v108, v75, v74, vcc
	v_div_scale_f32 v109, s[0:1], v108, v108, 1.0
	v_rcp_f32_e32 v110, v109
	s_lshl_b64 s[0:1], s[8:9], 13
	v_lshlrev_b32_e32 v74, 16, v76
	v_and_b32_e32 v75, 0xffff0000, v76
	v_fma_f32 v111, -v109, v110, 1.0
	v_fmac_f32_e32 v110, v111, v110
	v_div_scale_f32 v111, vcc, 1.0, v108, 1.0
	v_mul_f32_e32 v112, v111, v110
	v_fma_f32 v113, -v109, v112, v111
	v_fmac_f32_e32 v112, v113, v110
	v_fma_f32 v109, -v109, v112, v111
	v_div_fmas_f32 v109, v109, v110, v112
	ds_read_b128 v[112:115], v1
	ds_read_b128 v[116:119], v1 offset:16384
	v_div_fixup_f32 v110, v109, v108, 1.0
	v_pk_mul_f32 v[124:125], v[110:111], v[70:71] op_sel_hi:[0,1]
	v_pk_mul_f32 v[126:127], v[110:111], v[72:73] op_sel_hi:[0,1]
	ds_read_b128 v[70:73], v1 offset:1024
	ds_read_b128 v[120:123], v1 offset:17408
	s_waitcnt lgkmcnt(2)
	v_pk_fma_f32 v[112:113], v[112:113], v[124:125], v[116:117]
	v_pk_fma_f32 v[114:115], v[114:115], v[126:127], v[118:119]
	v_mul_f32_e32 v111, 0x41800000, v112
	v_mul_f32_e32 v112, 0x41800000, v113
	v_med3_f32 v111, v111, s17, v147
	v_med3_f32 v112, v112, s17, v147
	v_mov_b32_e32 v124, 0
	v_cvt_pk_fp8_f32 v124, v111, v112
	v_mul_f32_e32 v111, 0x41800000, v115
	v_med3_f32 v111, v111, s17, v147
	v_pk_mul_f32 v[66:67], v[110:111], v[66:67] op_sel_hi:[0,1]
	v_mul_f32_e32 v113, 0x41800000, v114
	s_waitcnt lgkmcnt(0)
	v_pk_fma_f32 v[66:67], v[70:71], v[66:67], v[120:121]
	v_med3_f32 v112, v113, s17, v147
	v_mul_f32_e32 v66, 0x41800000, v66
	v_mul_f32_e32 v67, 0x41800000, v67
	v_cvt_pk_fp8_f32 v124, v112, v111 op_sel:[0,0,1]
	v_pk_mul_f32 v[68:69], v[110:111], v[68:69] op_sel_hi:[0,1]
	v_med3_f32 v66, v66, s17, v147
	v_med3_f32 v67, v67, s17, v147
	v_mov_b32_e32 v111, 0
	v_cvt_pk_fp8_f32 v111, v66, v67
	v_pk_fma_f32 v[68:69], v[72:73], v[68:69], v[122:123]
	v_lshl_add_u64 v[108:109], v[4:5], 0, s[12:13]
	v_mul_f32_e32 v68, 0x41800000, v68
	v_mul_f32_e32 v66, 0x41800000, v69
	v_med3_f32 v67, v68, s17, v147
	v_med3_f32 v66, v66, s17, v147
	v_cvt_pk_fp8_f32 v111, v67, v66 op_sel:[0,0,1]
	ds_read_b128 v[66:69], v1 offset:2048
	ds_read_b128 v[70:73], v1 offset:18432
	v_lshlrev_b32_e32 v76, 16, v77
	v_and_b32_e32 v77, 0xffff0000, v77
	v_pk_mul_f32 v[116:117], v[110:111], v[62:63] op_sel_hi:[0,1]
	v_pk_mul_f32 v[118:119], v[110:111], v[64:65] op_sel_hi:[0,1]
	ds_read_b128 v[62:65], v1 offset:3072
	ds_read_b128 v[112:115], v1 offset:19456
	s_waitcnt lgkmcnt(2)
	v_pk_fma_f32 v[66:67], v[116:117], v[66:67], v[70:71]
	v_pk_mul_f32 v[58:59], v[110:111], v[58:59] op_sel_hi:[0,1]
	v_mul_f32_e32 v66, 0x41800000, v66
	v_mul_f32_e32 v67, 0x41800000, v67
	s_waitcnt lgkmcnt(0)
	v_pk_fma_f32 v[58:59], v[58:59], v[62:63], v[112:113]
	v_med3_f32 v66, v66, s17, v147
	v_med3_f32 v67, v67, s17, v147
	v_mov_b32_e32 v70, 0
	v_mul_f32_e32 v58, 0x41800000, v58
	v_mul_f32_e32 v59, 0x41800000, v59
	v_cvt_pk_fp8_f32 v70, v66, v67
	v_med3_f32 v58, v58, s17, v147
	v_med3_f32 v59, v59, s17, v147
	v_mov_b32_e32 v62, 0
	v_pk_fma_f32 v[68:69], v[118:119], v[68:69], v[72:73]
	v_pk_mul_f32 v[60:61], v[110:111], v[60:61] op_sel_hi:[0,1]
	v_cvt_pk_fp8_f32 v62, v58, v59
	v_mul_f32_e32 v68, 0x41800000, v68
	v_mul_f32_e32 v66, 0x41800000, v69
	v_pk_fma_f32 v[60:61], v[60:61], v[64:65], v[114:115]
	v_med3_f32 v67, v68, s17, v147
	v_med3_f32 v66, v66, s17, v147
	v_mul_f32_e32 v60, 0x41800000, v60
	v_mul_f32_e32 v58, 0x41800000, v61
	v_cvt_pk_fp8_f32 v70, v67, v66 op_sel:[0,0,1]
	v_med3_f32 v59, v60, s17, v147
	v_med3_f32 v58, v58, s17, v147
	v_cvt_pk_fp8_f32 v62, v59, v58 op_sel:[0,0,1]
	global_store_dword v[108:109], v124, off
	global_store_dword v[108:109], v111, off offset:256
	global_store_dword v[108:109], v70, off offset:512
	global_store_dword v[108:109], v62, off offset:768
	ds_read_b128 v[58:61], v1 offset:4096
	ds_read_b128 v[62:65], v1 offset:20480
	v_pk_mul_f32 v[70:71], v[110:111], v[54:55] op_sel_hi:[0,1]
	v_pk_mul_f32 v[72:73], v[110:111], v[56:57] op_sel_hi:[0,1]
	ds_read_b128 v[54:57], v1 offset:5120
	ds_read_b128 v[66:69], v1 offset:21504
	v_pk_mul_f32 v[50:51], v[110:111], v[50:51] op_sel_hi:[0,1]
	s_waitcnt lgkmcnt(2)
	v_pk_fma_f32 v[58:59], v[70:71], v[58:59], v[62:63]
	v_mov_b32_e32 v70, 0
	v_mul_f32_e32 v58, 0x41800000, v58
	s_waitcnt lgkmcnt(0)
	v_pk_fma_f32 v[50:51], v[50:51], v[54:55], v[66:67]
	v_mul_f32_e32 v59, 0x41800000, v59
	v_mul_f32_e32 v50, 0x41800000, v50
	v_mul_f32_e32 v51, 0x41800000, v51
	v_med3_f32 v50, v50, s17, v147
	v_med3_f32 v51, v51, s17, v147
	v_mov_b32_e32 v66, 0
	v_med3_f32 v58, v58, s17, v147
	v_med3_f32 v59, v59, s17, v147
	v_pk_mul_f32 v[52:53], v[110:111], v[52:53] op_sel_hi:[0,1]
	v_cvt_pk_fp8_f32 v66, v50, v51
	v_cvt_pk_fp8_f32 v70, v58, v59
	v_pk_fma_f32 v[52:53], v[52:53], v[56:57], v[68:69]
	v_pk_fma_f32 v[60:61], v[72:73], v[60:61], v[64:65]
	v_mul_f32_e32 v52, 0x41800000, v52
	v_mul_f32_e32 v50, 0x41800000, v53
	v_mul_f32_e32 v60, 0x41800000, v60
	v_mul_f32_e32 v58, 0x41800000, v61
	v_med3_f32 v51, v52, s17, v147
	v_med3_f32 v50, v50, s17, v147
	v_med3_f32 v59, v60, s17, v147
	v_med3_f32 v58, v58, s17, v147
	v_cvt_pk_fp8_f32 v66, v51, v50 op_sel:[0,0,1]
	ds_read_b128 v[50:53], v1 offset:6144
	ds_read_b128 v[54:57], v1 offset:22528
	v_cvt_pk_fp8_f32 v70, v59, v58 op_sel:[0,0,1]
	v_pk_mul_f32 v[62:63], v[110:111], v[46:47] op_sel_hi:[0,1]
	v_pk_mul_f32 v[64:65], v[110:111], v[48:49] op_sel_hi:[0,1]
	ds_read_b128 v[46:49], v1 offset:7168
	ds_read_b128 v[58:61], v1 offset:23552
	s_waitcnt lgkmcnt(2)
	v_pk_fma_f32 v[50:51], v[62:63], v[50:51], v[54:55]
	v_pk_mul_f32 v[42:43], v[110:111], v[42:43] op_sel_hi:[0,1]
	v_mul_f32_e32 v50, 0x41800000, v50
	v_mul_f32_e32 v51, 0x41800000, v51
	s_waitcnt lgkmcnt(0)
	v_pk_fma_f32 v[42:43], v[42:43], v[46:47], v[58:59]
	v_med3_f32 v50, v50, s17, v147
	v_med3_f32 v51, v51, s17, v147
	v_mov_b32_e32 v54, 0
	v_mul_f32_e32 v42, 0x41800000, v42
	v_mul_f32_e32 v43, 0x41800000, v43
	v_cvt_pk_fp8_f32 v54, v50, v51
	v_med3_f32 v42, v42, s17, v147
	v_med3_f32 v43, v43, s17, v147
	v_mov_b32_e32 v46, 0
	v_pk_fma_f32 v[52:53], v[64:65], v[52:53], v[56:57]
	v_pk_mul_f32 v[44:45], v[110:111], v[44:45] op_sel_hi:[0,1]
	v_cvt_pk_fp8_f32 v46, v42, v43
	v_mul_f32_e32 v52, 0x41800000, v52
	v_mul_f32_e32 v50, 0x41800000, v53
	v_pk_fma_f32 v[44:45], v[44:45], v[48:49], v[60:61]
	v_med3_f32 v51, v52, s17, v147
	v_med3_f32 v50, v50, s17, v147
	v_mul_f32_e32 v44, 0x41800000, v44
	v_mul_f32_e32 v42, 0x41800000, v45
	v_cvt_pk_fp8_f32 v54, v51, v50 op_sel:[0,0,1]
	v_med3_f32 v43, v44, s17, v147
	v_med3_f32 v42, v42, s17, v147
	v_cvt_pk_fp8_f32 v46, v43, v42 op_sel:[0,0,1]
	global_store_dword v[108:109], v70, off offset:1024
	global_store_dword v[108:109], v66, off offset:1280
	global_store_dword v[108:109], v54, off offset:1536
	global_store_dword v[108:109], v46, off offset:1792
	ds_read_b128 v[42:45], v1 offset:8192
	ds_read_b128 v[46:49], v1 offset:24576
	v_pk_mul_f32 v[54:55], v[110:111], v[38:39] op_sel_hi:[0,1]
	v_pk_mul_f32 v[56:57], v[110:111], v[40:41] op_sel_hi:[0,1]
	ds_read_b128 v[38:41], v1 offset:9216
	ds_read_b128 v[50:53], v1 offset:25600
	v_pk_mul_f32 v[34:35], v[110:111], v[34:35] op_sel_hi:[0,1]
	s_waitcnt lgkmcnt(2)
	v_pk_fma_f32 v[42:43], v[54:55], v[42:43], v[46:47]
	v_mov_b32_e32 v54, 0
	v_mul_f32_e32 v42, 0x41800000, v42
	s_waitcnt lgkmcnt(0)
	v_pk_fma_f32 v[34:35], v[34:35], v[38:39], v[50:51]
	v_mul_f32_e32 v43, 0x41800000, v43
	v_mul_f32_e32 v34, 0x41800000, v34
	v_mul_f32_e32 v35, 0x41800000, v35
	v_med3_f32 v34, v34, s17, v147
	v_med3_f32 v35, v35, s17, v147
	v_mov_b32_e32 v50, 0
	v_med3_f32 v42, v42, s17, v147
	v_med3_f32 v43, v43, s17, v147
	v_pk_mul_f32 v[36:37], v[110:111], v[36:37] op_sel_hi:[0,1]
	v_cvt_pk_fp8_f32 v50, v34, v35
	v_cvt_pk_fp8_f32 v54, v42, v43
	v_pk_fma_f32 v[36:37], v[36:37], v[40:41], v[52:53]
	v_pk_fma_f32 v[44:45], v[56:57], v[44:45], v[48:49]
	v_mul_f32_e32 v36, 0x41800000, v36
	v_mul_f32_e32 v34, 0x41800000, v37
	v_mul_f32_e32 v44, 0x41800000, v44
	v_mul_f32_e32 v42, 0x41800000, v45
	v_med3_f32 v35, v36, s17, v147
	v_med3_f32 v34, v34, s17, v147
	v_med3_f32 v43, v44, s17, v147
	v_med3_f32 v42, v42, s17, v147
	v_cvt_pk_fp8_f32 v50, v35, v34 op_sel:[0,0,1]
	ds_read_b128 v[34:37], v1 offset:10240
	ds_read_b128 v[38:41], v1 offset:26624
	v_cvt_pk_fp8_f32 v54, v43, v42 op_sel:[0,0,1]
	v_pk_mul_f32 v[46:47], v[110:111], v[28:29] op_sel_hi:[0,1]
	v_pk_mul_f32 v[48:49], v[110:111], v[30:31] op_sel_hi:[0,1]
	ds_read_b128 v[28:31], v1 offset:11264
	ds_read_b128 v[42:45], v1 offset:27648
	s_waitcnt lgkmcnt(2)
	v_pk_fma_f32 v[34:35], v[46:47], v[34:35], v[38:39]
	v_pk_mul_f32 v[20:21], v[110:111], v[20:21] op_sel_hi:[0,1]
	v_mul_f32_e32 v34, 0x41800000, v34
	v_mul_f32_e32 v35, 0x41800000, v35
	s_waitcnt lgkmcnt(0)
	v_pk_fma_f32 v[20:21], v[20:21], v[28:29], v[42:43]
	v_med3_f32 v34, v34, s17, v147
	v_med3_f32 v35, v35, s17, v147
	v_mov_b32_e32 v38, 0
	v_mul_f32_e32 v20, 0x41800000, v20
	v_mul_f32_e32 v21, 0x41800000, v21
	v_cvt_pk_fp8_f32 v38, v34, v35
	v_med3_f32 v20, v20, s17, v147
	v_med3_f32 v21, v21, s17, v147
	v_mov_b32_e32 v28, 0
	v_pk_fma_f32 v[36:37], v[48:49], v[36:37], v[40:41]
	v_pk_mul_f32 v[22:23], v[110:111], v[22:23] op_sel_hi:[0,1]
	v_cvt_pk_fp8_f32 v28, v20, v21
	v_mul_f32_e32 v36, 0x41800000, v36
	v_mul_f32_e32 v34, 0x41800000, v37
	v_pk_fma_f32 v[22:23], v[22:23], v[30:31], v[44:45]
	v_med3_f32 v35, v36, s17, v147
	v_med3_f32 v34, v34, s17, v147
	v_mul_f32_e32 v22, 0x41800000, v22
	v_mul_f32_e32 v20, 0x41800000, v23
	v_cvt_pk_fp8_f32 v38, v35, v34 op_sel:[0,0,1]
	v_med3_f32 v21, v22, s17, v147
	v_med3_f32 v20, v20, s17, v147
	v_cvt_pk_fp8_f32 v28, v21, v20 op_sel:[0,0,1]
	global_store_dword v[108:109], v54, off offset:2048
	global_store_dword v[108:109], v50, off offset:2304
	global_store_dword v[108:109], v38, off offset:2560
	global_store_dword v[108:109], v28, off offset:2816
	ds_read_b128 v[20:23], v1 offset:12288
	ds_read_b128 v[28:31], v1 offset:28672
	v_pk_mul_f32 v[38:39], v[110:111], v[16:17] op_sel_hi:[0,1]
	v_pk_mul_f32 v[40:41], v[110:111], v[18:19] op_sel_hi:[0,1]
	ds_read_b128 v[16:19], v1 offset:13312
	ds_read_b128 v[34:37], v1 offset:14336
	v_pk_mul_f32 v[10:11], v[110:111], v[10:11] op_sel_hi:[0,1]
	s_waitcnt lgkmcnt(2)
;     ...
;         NR_LOAD(va, m0); NR_LOAD(vb, m0 + 1); NR_FIN(va, m0); NR_LOAD(va, m0 + 2); NR_FIN(vb, m0 + 1); NR_LOAD(vb, m0 + 3); NR_FIN(va, m0 + 2); NR_FIN(vb, m0 + 3);
	v_pk_fma_f32 v[20:21], v[38:39], v[20:21], v[28:29]
	v_pk_fma_f32 v[22:23], v[40:41], v[22:23], v[30:31]
	v_mul_f32_e32 v20, 0x41800000, v20
	v_mul_f32_e32 v21, 0x41800000, v21
	v_mul_f32_e32 v22, 0x41800000, v22
	v_mul_f32_e32 v23, 0x41800000, v23
	v_med3_f32 v20, v20, s17, v147
	v_med3_f32 v21, v21, s17, v147
	v_mov_b32_e32 v38, 0
	v_cvt_pk_fp8_f32 v38, v20, v21
	v_med3_f32 v28, v22, s17, v147
	v_med3_f32 v29, v23, s17, v147
	ds_read_b128 v[20:23], v1 offset:29696
	v_cvt_pk_fp8_f32 v38, v28, v29 op_sel:[0,0,1]
	v_pk_mul_f32 v[28:29], v[110:111], v[12:13] op_sel_hi:[0,1]
	v_pk_mul_f32 v[30:31], v[110:111], v[14:15] op_sel_hi:[0,1]
	ds_read_b128 v[12:15], v1 offset:30720
	s_waitcnt lgkmcnt(1)
	v_pk_fma_f32 v[16:17], v[28:29], v[16:17], v[20:21]
	v_pk_fma_f32 v[18:19], v[30:31], v[18:19], v[22:23]
	v_mul_f32_e32 v16, 0x41800000, v16
	v_mul_f32_e32 v17, 0x41800000, v17
	v_med3_f32 v16, v16, s17, v147
	v_med3_f32 v17, v17, s17, v147
	v_mov_b32_e32 v22, 0
	v_cvt_pk_fp8_f32 v22, v16, v17
	v_mul_f32_e32 v18, 0x41800000, v18
	v_mul_f32_e32 v16, 0x41800000, v19
	v_med3_f32 v17, v18, s17, v147
	v_med3_f32 v16, v16, s17, v147
	v_cvt_pk_fp8_f32 v22, v17, v16 op_sel:[0,0,1]
	v_pk_mul_f32 v[16:17], v[110:111], v[32:33] op_sel_hi:[0,1]
	s_waitcnt lgkmcnt(0)
	v_pk_fma_f32 v[10:11], v[10:11], v[34:35], v[12:13]
	v_pk_fma_f32 v[14:15], v[16:17], v[36:37], v[14:15]
	v_mul_f32_e32 v10, 0x41800000, v10
	v_mul_f32_e32 v11, 0x41800000, v11
	v_mul_f32_e32 v12, 0x41800000, v14
	v_med3_f32 v10, v10, s17, v147
	v_med3_f32 v11, v11, s17, v147
	v_mov_b32_e32 v23, 0
	v_mul_f32_e32 v18, 0x41800000, v15
	v_cvt_pk_fp8_f32 v23, v10, v11
	v_med3_f32 v19, v12, s17, v147
	ds_read_b128 v[10:13], v142
	ds_read_b128 v[14:17], v142 offset:16384
	v_med3_f32 v18, v18, s17, v147
	v_cvt_pk_fp8_f32 v23, v19, v18 op_sel:[0,0,1]
	v_pk_mul_f32 v[18:19], v[110:111], v[24:25] op_sel_hi:[0,1]
	v_pk_mul_f32 v[20:21], v[110:111], v[26:27] op_sel_hi:[0,1]
	s_waitcnt lgkmcnt(0)
	v_pk_fma_f32 v[10:11], v[18:19], v[10:11], v[14:15]
	v_mov_b32_e32 v14, 0
	v_mul_f32_e32 v10, 0x41800000, v10
	v_mul_f32_e32 v11, 0x41800000, v11
	v_med3_f32 v10, v10, s17, v147
	v_med3_f32 v11, v11, s17, v147
	v_cvt_pk_fp8_f32 v14, v10, v11
	v_pk_fma_f32 v[12:13], v[20:21], v[12:13], v[16:17]
	v_and_b32_e32 v127, 0xffff0000, v100
	v_mul_f32_e32 v12, 0x41800000, v12
	v_mul_f32_e32 v10, 0x41800000, v13
	v_med3_f32 v11, v12, s17, v147
	v_med3_f32 v10, v10, s17, v147
	v_cvt_pk_fp8_f32 v14, v11, v10 op_sel:[0,0,1]
	global_store_dword v[108:109], v38, off offset:3072
	global_store_dword v[108:109], v22, off offset:3328
	global_store_dword v[108:109], v23, off offset:3584
	global_store_dword v[108:109], v14, off offset:3840
	v_lshl_add_u64 v[10:11], v[2:3], 0, s[0:1]
	global_load_dwordx2 v[12:13], v[10:11], off nt
	global_load_dwordx2 v[14:15], v[10:11], off offset:512 nt
	global_load_dwordx2 v[16:17], v[10:11], off offset:1024 nt
	global_load_dwordx2 v[18:19], v[10:11], off offset:1536 nt
	global_load_dwordx2 v[20:21], v[10:11], off offset:2048 nt
	global_load_dwordx2 v[22:23], v[10:11], off offset:2560 nt
	global_load_dwordx2 v[24:25], v[10:11], off offset:3072 nt
	global_load_dwordx2 v[26:27], v[10:11], off offset:3584 nt
	v_add_co_u32_e32 v10, vcc, s15, v10
	v_lshlrev_b32_e32 v126, 16, v100
	s_nop 0
	v_addc_co_u32_e32 v11, vcc, 0, v11, vcc
	global_load_dwordx2 v[28:29], v[10:11], off nt
	global_load_dwordx2 v[30:31], v[10:11], off offset:512 nt
	global_load_dwordx2 v[32:33], v[10:11], off offset:1024 nt
	global_load_dwordx2 v[148:149], v[10:11], off offset:1536 nt
	global_load_dwordx2 v[150:151], v[10:11], off offset:2048 nt
	global_load_dwordx2 v[152:153], v[10:11], off offset:2560 nt
	global_load_dwordx2 v[154:155], v[10:11], off offset:3072 nt
	v_and_b32_e32 v123, 0xffff0000, v98
	v_and_b32_e32 v125, 0xffff0000, v99
	v_lshlrev_b32_e32 v122, 16, v98
	v_lshlrev_b32_e32 v124, 16, v99
	v_and_b32_e32 v119, 0xffff0000, v96
	v_and_b32_e32 v121, 0xffff0000, v97
	v_lshlrev_b32_e32 v118, 16, v96
	v_lshlrev_b32_e32 v120, 16, v97
	v_and_b32_e32 v115, 0xffff0000, v92
	v_and_b32_e32 v117, 0xffff0000, v93
	v_lshlrev_b32_e32 v114, 16, v92
	v_lshlrev_b32_e32 v116, 16, v93
	v_and_b32_e32 v111, 0xffff0000, v94
	v_and_b32_e32 v113, 0xffff0000, v95
	v_lshlrev_b32_e32 v110, 16, v94
	v_lshlrev_b32_e32 v112, 16, v95
	v_and_b32_e32 v109, 0xffff0000, v87
	v_lshlrev_b32_e32 v108, 16, v87
	s_waitcnt vmcnt(36)
	v_and_b32_e32 v103, 0xffff0000, v78
	v_and_b32_e32 v105, 0xffff0000, v79
	v_lshlrev_b32_e32 v102, 16, v78
	v_lshlrev_b32_e32 v104, 16, v79
	s_waitcnt vmcnt(35)
	v_and_b32_e32 v99, 0xffff0000, v80
	v_and_b32_e32 v101, 0xffff0000, v81
	v_lshlrev_b32_e32 v98, 16, v80
	v_lshlrev_b32_e32 v100, 16, v81
	s_waitcnt vmcnt(34)
	v_and_b32_e32 v95, 0xffff0000, v82
	v_and_b32_e32 v97, 0xffff0000, v83
	v_lshlrev_b32_e32 v94, 16, v82
	v_lshlrev_b32_e32 v96, 16, v83
	s_waitcnt vmcnt(33)
	v_and_b32_e32 v87, 0xffff0000, v84
	v_and_b32_e32 v93, 0xffff0000, v85
	v_lshlrev_b32_e32 v86, 16, v84
	v_lshlrev_b32_e32 v92, 16, v85
	s_waitcnt vmcnt(32)
	v_and_b32_e32 v83, 0xffff0000, v88
	v_and_b32_e32 v85, 0xffff0000, v89
	v_lshlrev_b32_e32 v82, 16, v88
	v_lshlrev_b32_e32 v84, 16, v89
	s_waitcnt vmcnt(31)
	v_and_b32_e32 v79, 0xffff0000, v90
	v_and_b32_e32 v81, 0xffff0000, v91
	v_lshlrev_b32_e32 v78, 16, v90
	v_lshlrev_b32_e32 v80, 16, v91
	s_waitcnt vmcnt(14)
	v_lshlrev_b32_e32 v70, 16, v12
	v_and_b32_e32 v71, 0xffff0000, v12
	v_lshlrev_b32_e32 v72, 16, v13
	v_and_b32_e32 v73, 0xffff0000, v13
	s_waitcnt vmcnt(10)
	v_lshlrev_b32_e32 v54, 16, v20
	v_and_b32_e32 v55, 0xffff0000, v20
	s_waitcnt vmcnt(8)
	v_lshlrev_b32_e32 v46, 16, v24
	v_and_b32_e32 v47, 0xffff0000, v24
	v_lshlrev_b32_e32 v48, 16, v25
	v_and_b32_e32 v49, 0xffff0000, v25
	v_mul_f32_e32 v24, v75, v75
	v_mul_f32_e32 v25, v77, v77
	v_fmac_f32_e32 v24, v74, v74
	v_fmac_f32_e32 v25, v76, v76
	s_waitcnt vmcnt(6)
	v_lshlrev_b32_e32 v38, 16, v28
	v_and_b32_e32 v39, 0xffff0000, v28
	v_lshlrev_b32_e32 v40, 16, v29
	v_and_b32_e32 v41, 0xffff0000, v29
	s_waitcnt vmcnt(4)
	v_lshlrev_b32_e32 v28, 16, v32
	v_and_b32_e32 v29, 0xffff0000, v32
	v_add_f32_e32 v24, v24, v25
	v_mul_f32_e32 v25, v139, v139
	v_mul_f32_e32 v32, v141, v141
	v_fmac_f32_e32 v25, v138, v138
	v_fmac_f32_e32 v32, v140, v140
	v_add_f32_e32 v25, v25, v32
	v_add_f32_e32 v24, v24, v25
	v_mul_f32_e32 v25, v135, v135
	v_mul_f32_e32 v32, v137, v137
	v_fmac_f32_e32 v25, v134, v134
	v_fmac_f32_e32 v32, v136, v136
	v_add_f32_e32 v25, v25, v32
	v_add_f32_e32 v24, v24, v25
	v_mul_f32_e32 v25, v131, v131
	v_mul_f32_e32 v32, v133, v133
	v_fmac_f32_e32 v25, v130, v130
	v_fmac_f32_e32 v32, v132, v132
	v_add_f32_e32 v25, v25, v32
	v_add_f32_e32 v24, v24, v25
	v_mul_f32_e32 v25, v127, v127
	v_mul_f32_e32 v32, v129, v129
	v_fmac_f32_e32 v25, v126, v126
	v_fmac_f32_e32 v32, v128, v128
	v_add_f32_e32 v25, v25, v32
	v_add_f32_e32 v24, v24, v25
	v_mul_f32_e32 v25, v123, v123
	v_mul_f32_e32 v32, v125, v125
	v_fmac_f32_e32 v25, v122, v122
	v_fmac_f32_e32 v32, v124, v124
	v_add_f32_e32 v25, v25, v32
	v_add_f32_e32 v24, v24, v25
	v_mul_f32_e32 v25, v119, v119
	v_mul_f32_e32 v32, v121, v121
	v_fmac_f32_e32 v25, v118, v118
	v_fmac_f32_e32 v32, v120, v120
	v_add_f32_e32 v25, v25, v32
	v_add_f32_e32 v24, v24, v25
	v_mul_f32_e32 v25, v115, v115
	v_mul_f32_e32 v32, v117, v117
	v_fmac_f32_e32 v25, v114, v114
	v_fmac_f32_e32 v32, v116, v116
	v_add_f32_e32 v25, v25, v32
	v_add_f32_e32 v24, v24, v25
	v_mul_f32_e32 v25, v111, v111
	v_mul_f32_e32 v32, v113, v113
	v_fmac_f32_e32 v25, v110, v110
	v_fmac_f32_e32 v32, v112, v112
	v_add_f32_e32 v25, v25, v32
	v_add_f32_e32 v24, v24, v25
	v_mul_f32_e32 v25, v107, v107
	v_mul_f32_e32 v32, v109, v109
	v_fmac_f32_e32 v25, v106, v106
	v_fmac_f32_e32 v32, v108, v108
	v_add_f32_e32 v25, v25, v32
	v_add_f32_e32 v24, v24, v25
	v_mul_f32_e32 v25, v103, v103
	v_mul_f32_e32 v32, v105, v105
	v_fmac_f32_e32 v25, v102, v102
	v_fmac_f32_e32 v32, v104, v104
	v_add_f32_e32 v25, v25, v32
	v_add_f32_e32 v24, v24, v25
	v_mul_f32_e32 v25, v99, v99
	v_mul_f32_e32 v32, v101, v101
	v_fmac_f32_e32 v25, v98, v98
	v_fmac_f32_e32 v32, v100, v100
	v_add_f32_e32 v25, v25, v32
	v_add_f32_e32 v24, v24, v25
	v_mul_f32_e32 v25, v95, v95
	v_mul_f32_e32 v32, v97, v97
	v_fmac_f32_e32 v25, v94, v94
	v_fmac_f32_e32 v32, v96, v96
	v_add_f32_e32 v25, v25, v32
	v_add_f32_e32 v24, v24, v25
	v_mul_f32_e32 v25, v87, v87
	v_mul_f32_e32 v32, v93, v93
	v_fmac_f32_e32 v25, v86, v86
	v_fmac_f32_e32 v32, v92, v92
	v_add_f32_e32 v25, v25, v32
	v_add_f32_e32 v24, v24, v25
	v_mul_f32_e32 v25, v83, v83
	v_mul_f32_e32 v32, v85, v85
	v_fmac_f32_e32 v25, v82, v82
	v_fmac_f32_e32 v32, v84, v84
	v_add_f32_e32 v25, v25, v32
	v_add_f32_e32 v24, v24, v25
	v_mul_f32_e32 v25, v79, v79
	v_mul_f32_e32 v32, v81, v81
	v_fmac_f32_e32 v25, v78, v78
	v_fmac_f32_e32 v32, v80, v80
	v_add_f32_e32 v25, v25, v32
	v_add_f32_e32 v24, v24, v25
	v_lshlrev_b32_e32 v42, 16, v26
	v_and_b32_e32 v43, 0xffff0000, v26
	v_add_f32_dpp v24, v24, v24 quad_perm:[1,0,3,2] row_mask:0xf bank_mask:0xf bound_ctrl:1
	v_lshlrev_b32_e32 v44, 16, v27
	v_and_b32_e32 v45, 0xffff0000, v27
	v_add_f32_dpp v24, v24, v24 quad_perm:[2,3,0,1] row_mask:0xf bank_mask:0xf bound_ctrl:1
	global_load_dwordx2 v[26:27], v[10:11], off offset:3584 nt
	v_lshlrev_b32_e32 v56, 16, v21
	v_add_f32_dpp v24, v24, v24 row_half_mirror row_mask:0xf bank_mask:0xf bound_ctrl:1
	v_and_b32_e32 v57, 0xffff0000, v21
	s_waitcnt vmcnt(4)
	v_lshlrev_b32_e32 v20, 16, v148
	v_add_f32_dpp v24, v24, v24 row_mirror row_mask:0xf bank_mask:0xf bound_ctrl:1
	v_mov_b32_e32 v25, v24
	s_nop 1
	v_permlane16_swap_b32 v24, v25
	v_and_b32_e32 v21, 0xffff0000, v148
	v_add_f32_e32 v24, v24, v25
	v_mov_b32_e32 v25, v24
	s_nop 1
	v_permlane32_swap_b32 v24, v25
	v_lshlrev_b32_e32 v50, 16, v22
	v_add_f32_e32 v24, v24, v25
	v_fmamk_f32 v24, v24, 0x39800000, v145
	v_mul_f32_e32 v25, 0x4f800000, v24
	v_cmp_gt_f32_e32 vcc, s16, v24
	v_and_b32_e32 v51, 0xffff0000, v22
	v_lshlrev_b32_e32 v52, 16, v23
	v_cndmask_b32_e32 v25, v24, v25, vcc
	v_sqrt_f32_e32 v88, v25
	v_and_b32_e32 v53, 0xffff0000, v23
	v_lshlrev_b32_e32 v22, 16, v149
	v_and_b32_e32 v23, 0xffff0000, v149
	v_add_u32_e32 v89, -1, v88
	v_fma_f32 v90, -v89, v88, v25
	v_cmp_ge_f32_e64 s[0:1], 0, v90
	v_add_u32_e32 v90, 1, v88
	v_lshlrev_b32_e32 v66, 16, v14
	v_cndmask_b32_e64 v89, v88, v89, s[0:1]
	v_fma_f32 v88, -v90, v88, v25
	v_cmp_lt_f32_e64 s[0:1], 0, v88
	v_and_b32_e32 v67, 0xffff0000, v14
	v_lshlrev_b32_e32 v68, 16, v15
	v_cndmask_b32_e64 v88, v89, v90, s[0:1]
	v_mul_f32_e32 v89, 0x37800000, v88
	v_cndmask_b32_e32 v88, v88, v89, vcc
	v_cmp_class_f32_e32 vcc, v25, v146
	v_and_b32_e32 v69, 0xffff0000, v15
	v_lshlrev_b32_e32 v62, 16, v16
	v_cndmask_b32_e32 v88, v88, v25, vcc
	v_div_scale_f32 v89, s[0:1], v88, v88, 1.0
	v_rcp_f32_e32 v90, v89
	v_and_b32_e32 v63, 0xffff0000, v16
	v_lshlrev_b32_e32 v64, 16, v17
	v_and_b32_e32 v65, 0xffff0000, v17
	v_fma_f32 v91, -v89, v90, 1.0
	v_fmac_f32_e32 v90, v91, v90
	v_div_scale_f32 v91, vcc, 1.0, v88, 1.0
	v_mul_f32_e32 v148, v91, v90
	v_fma_f32 v149, -v89, v148, v91
	v_fmac_f32_e32 v148, v149, v90
	v_fma_f32 v89, -v89, v148, v91
	v_lshlrev_b32_e32 v58, 16, v18
	v_and_b32_e32 v59, 0xffff0000, v18
	v_lshlrev_b32_e32 v60, 16, v19
	v_and_b32_e32 v61, 0xffff0000, v19
	v_lshlrev_b32_e32 v34, 16, v30
	v_and_b32_e32 v35, 0xffff0000, v30
	v_lshlrev_b32_e32 v36, 16, v31
	v_and_b32_e32 v37, 0xffff0000, v31
	v_lshlrev_b32_e32 v30, 16, v33
	v_and_b32_e32 v31, 0xffff0000, v33
	s_waitcnt vmcnt(3)
	v_lshlrev_b32_e32 v16, 16, v150
	v_and_b32_e32 v17, 0xffff0000, v150
	v_lshlrev_b32_e32 v18, 16, v151
	v_and_b32_e32 v19, 0xffff0000, v151
	s_waitcnt vmcnt(2)
	v_lshlrev_b32_e32 v12, 16, v152
	v_and_b32_e32 v13, 0xffff0000, v152
	v_lshlrev_b32_e32 v14, 16, v153
	v_and_b32_e32 v15, 0xffff0000, v153
	s_waitcnt vmcnt(1)
	v_lshlrev_b32_e32 v10, 16, v154
	v_and_b32_e32 v11, 0xffff0000, v154
	v_lshlrev_b32_e32 v32, 16, v155
	v_and_b32_e32 v33, 0xffff0000, v155
	v_div_fmas_f32 v89, v89, v90, v148
	ds_read_b128 v[148:151], v1
	ds_read_b128 v[152:155], v1 offset:16384
	v_div_fixup_f32 v90, v89, v88, 1.0
	v_pk_mul_f32 v[160:161], v[90:91], v[74:75] op_sel_hi:[0,1]
	v_pk_mul_f32 v[162:163], v[90:91], v[76:77] op_sel_hi:[0,1]
	ds_read_b128 v[74:77], v1 offset:1024
	ds_read_b128 v[156:159], v1 offset:17408
	s_waitcnt lgkmcnt(2)
	v_pk_fma_f32 v[148:149], v[148:149], v[160:161], v[152:153]
	v_pk_fma_f32 v[150:151], v[150:151], v[162:163], v[154:155]
	v_mul_f32_e32 v91, 0x41800000, v148
	v_mul_f32_e32 v148, 0x41800000, v149
	v_med3_f32 v91, v91, s17, v147
	v_med3_f32 v148, v148, s17, v147
	v_mov_b32_e32 v160, 0
	v_cvt_pk_fp8_f32 v160, v91, v148
	v_mul_f32_e32 v91, 0x41800000, v151
	v_med3_f32 v91, v91, s17, v147
	v_pk_mul_f32 v[138:139], v[90:91], v[138:139] op_sel_hi:[0,1]
	v_mul_f32_e32 v149, 0x41800000, v150
	s_waitcnt lgkmcnt(0)
	v_pk_fma_f32 v[74:75], v[74:75], v[138:139], v[156:157]
	v_med3_f32 v148, v149, s17, v147
	v_mul_f32_e32 v74, 0x41800000, v74
	v_mul_f32_e32 v75, 0x41800000, v75
	v_cvt_pk_fp8_f32 v160, v148, v91 op_sel:[0,0,1]
	v_pk_mul_f32 v[140:141], v[90:91], v[140:141] op_sel_hi:[0,1]
	v_med3_f32 v74, v74, s17, v147
	v_med3_f32 v75, v75, s17, v147
	v_mov_b32_e32 v91, 0
	v_cvt_pk_fp8_f32 v91, v74, v75
	v_pk_fma_f32 v[76:77], v[76:77], v[140:141], v[158:159]
	v_lshl_add_u64 v[88:89], v[4:5], 0, s[10:11]
	v_mul_f32_e32 v76, 0x41800000, v76
	v_mul_f32_e32 v74, 0x41800000, v77
	v_med3_f32 v75, v76, s17, v147
	v_med3_f32 v74, v74, s17, v147
	v_cvt_pk_fp8_f32 v91, v75, v74 op_sel:[0,0,1]
	ds_read_b128 v[74:77], v1 offset:2048
	ds_read_b128 v[138:141], v1 offset:18432
	s_waitcnt vmcnt(0)
	v_lshlrev_b32_e32 v24, 16, v26
	v_and_b32_e32 v25, 0xffff0000, v26
	v_pk_mul_f32 v[152:153], v[90:91], v[134:135] op_sel_hi:[0,1]
	v_pk_mul_f32 v[154:155], v[90:91], v[136:137] op_sel_hi:[0,1]
	s_waitcnt lgkmcnt(0)
	v_pk_fma_f32 v[74:75], v[152:153], v[74:75], v[138:139]
	v_mov_b32_e32 v138, 0
	v_mul_f32_e32 v74, 0x41800000, v74
	v_mul_f32_e32 v75, 0x41800000, v75
	v_med3_f32 v74, v74, s17, v147
	v_med3_f32 v75, v75, s17, v147
	ds_read_b128 v[134:137], v1 offset:3072
	ds_read_b128 v[148:151], v1 offset:19456
	v_cvt_pk_fp8_f32 v138, v74, v75
	v_pk_fma_f32 v[76:77], v[154:155], v[76:77], v[140:141]
	v_pk_mul_f32 v[140:141], v[90:91], v[128:129] op_sel_hi:[0,1]
	v_mul_f32_e32 v76, 0x41800000, v76
	v_mul_f32_e32 v74, 0x41800000, v77
	v_med3_f32 v75, v76, s17, v147
	v_med3_f32 v74, v74, s17, v147
	v_cvt_pk_fp8_f32 v138, v75, v74 op_sel:[0,0,1]
	v_pk_mul_f32 v[74:75], v[90:91], v[130:131] op_sel_hi:[0,1]
	s_waitcnt lgkmcnt(0)
	v_pk_fma_f32 v[74:75], v[74:75], v[134:135], v[148:149]
	v_mov_b32_e32 v130, 0
	v_mul_f32_e32 v74, 0x41800000, v74
	v_mul_f32_e32 v75, 0x41800000, v75
	v_med3_f32 v74, v74, s17, v147
	v_med3_f32 v75, v75, s17, v147
	v_pk_mul_f32 v[76:77], v[90:91], v[132:133] op_sel_hi:[0,1]
	v_cvt_pk_fp8_f32 v130, v74, v75
	v_pk_fma_f32 v[76:77], v[76:77], v[136:137], v[150:151]
	v_lshlrev_b32_e32 v26, 16, v27
	v_mul_f32_e32 v76, 0x41800000, v76
	v_mul_f32_e32 v74, 0x41800000, v77
	v_med3_f32 v75, v76, s17, v147
	v_med3_f32 v74, v74, s17, v147
	v_cvt_pk_fp8_f32 v130, v75, v74 op_sel:[0,0,1]
	global_store_dword v[88:89], v160, off
	global_store_dword v[88:89], v91, off offset:256
	global_store_dword v[88:89], v138, off offset:512
	global_store_dword v[88:89], v130, off offset:768
	ds_read_b128 v[74:77], v1 offset:4096
	ds_read_b128 v[130:133], v1 offset:20480
	v_pk_mul_f32 v[138:139], v[90:91], v[126:127] op_sel_hi:[0,1]
	v_mov_b32_e32 v91, 0
	ds_read_b128 v[126:129], v1 offset:5120
	ds_read_b128 v[134:137], v1 offset:21504
	v_and_b32_e32 v27, 0xffff0000, v27
	s_waitcnt lgkmcnt(2)
	v_pk_fma_f32 v[74:75], v[138:139], v[74:75], v[130:131]
	v_pk_fma_f32 v[76:77], v[140:141], v[76:77], v[132:133]
	v_mul_f32_e32 v74, 0x41800000, v74
	v_mul_f32_e32 v75, 0x41800000, v75
	v_med3_f32 v74, v74, s17, v147
	v_med3_f32 v75, v75, s17, v147
	v_cvt_pk_fp8_f32 v91, v74, v75
	v_mul_f32_e32 v76, 0x41800000, v76
	v_mul_f32_e32 v74, 0x41800000, v77
	v_med3_f32 v75, v76, s17, v147
	v_med3_f32 v74, v74, s17, v147
	v_cvt_pk_fp8_f32 v91, v75, v74 op_sel:[0,0,1]
	s_nop 0
	v_pk_mul_f32 v[74:75], v[90:91], v[122:123] op_sel_hi:[0,1]
	s_waitcnt lgkmcnt(0)
	v_pk_fma_f32 v[74:75], v[74:75], v[126:127], v[134:135]
	v_mov_b32_e32 v134, 0
	v_mul_f32_e32 v74, 0x41800000, v74
	v_mul_f32_e32 v75, 0x41800000, v75
	v_med3_f32 v74, v74, s17, v147
	v_med3_f32 v75, v75, s17, v147
	v_pk_mul_f32 v[76:77], v[90:91], v[124:125] op_sel_hi:[0,1]
	v_cvt_pk_fp8_f32 v134, v74, v75
	v_pk_fma_f32 v[76:77], v[76:77], v[128:129], v[136:137]
	v_pk_mul_f32 v[130:131], v[90:91], v[118:119] op_sel_hi:[0,1]
	v_mul_f32_e32 v76, 0x41800000, v76
	v_mul_f32_e32 v74, 0x41800000, v77
	v_med3_f32 v75, v76, s17, v147
	v_med3_f32 v74, v74, s17, v147
	v_cvt_pk_fp8_f32 v134, v75, v74 op_sel:[0,0,1]
	ds_read_b128 v[74:77], v1 offset:6144
	ds_read_b128 v[122:125], v1 offset:22528
	v_pk_mul_f32 v[132:133], v[90:91], v[120:121] op_sel_hi:[0,1]
	ds_read_b128 v[118:121], v1 offset:7168
	ds_read_b128 v[126:129], v1 offset:23552
	s_waitcnt lgkmcnt(2)
	v_pk_fma_f32 v[74:75], v[130:131], v[74:75], v[122:123]
	s_nop 0
	v_mul_f32_e32 v74, 0x41800000, v74
	v_mul_f32_e32 v75, 0x41800000, v75
	v_med3_f32 v74, v74, s17, v147
	v_med3_f32 v75, v75, s17, v147
	v_mov_b32_e32 v122, 0
	v_cvt_pk_fp8_f32 v122, v74, v75
	v_pk_fma_f32 v[76:77], v[132:133], v[76:77], v[124:125]
	v_pk_mul_f32 v[124:125], v[90:91], v[112:113] op_sel_hi:[0,1]
	v_mul_f32_e32 v76, 0x41800000, v76
	v_mul_f32_e32 v74, 0x41800000, v77
	v_med3_f32 v75, v76, s17, v147
	v_med3_f32 v74, v74, s17, v147
	v_cvt_pk_fp8_f32 v122, v75, v74 op_sel:[0,0,1]
	v_pk_mul_f32 v[74:75], v[90:91], v[114:115] op_sel_hi:[0,1]
	s_waitcnt lgkmcnt(0)
	v_pk_fma_f32 v[74:75], v[74:75], v[118:119], v[126:127]
	v_mov_b32_e32 v114, 0
	v_mul_f32_e32 v74, 0x41800000, v74
	v_mul_f32_e32 v75, 0x41800000, v75
	v_med3_f32 v74, v74, s17, v147
	v_med3_f32 v75, v75, s17, v147
	v_pk_mul_f32 v[76:77], v[90:91], v[116:117] op_sel_hi:[0,1]
	v_cvt_pk_fp8_f32 v114, v74, v75
	v_pk_fma_f32 v[76:77], v[76:77], v[120:121], v[128:129]
	s_nop 0
	v_mul_f32_e32 v76, 0x41800000, v76
	v_mul_f32_e32 v74, 0x41800000, v77
	v_med3_f32 v75, v76, s17, v147
	v_med3_f32 v74, v74, s17, v147
	v_cvt_pk_fp8_f32 v114, v75, v74 op_sel:[0,0,1]
	global_store_dword v[88:89], v91, off offset:1024
	global_store_dword v[88:89], v134, off offset:1280
	global_store_dword v[88:89], v122, off offset:1536
	global_store_dword v[88:89], v114, off offset:1792
	ds_read_b128 v[74:77], v1 offset:8192
	ds_read_b128 v[114:117], v1 offset:24576
	v_pk_mul_f32 v[122:123], v[90:91], v[110:111] op_sel_hi:[0,1]
	v_mov_b32_e32 v91, 0
	ds_read_b128 v[110:113], v1 offset:9216
	ds_read_b128 v[118:121], v1 offset:25600
	s_waitcnt lgkmcnt(2)
	v_pk_fma_f32 v[74:75], v[122:123], v[74:75], v[114:115]
	s_nop 0
	v_mul_f32_e32 v74, 0x41800000, v74
	v_mul_f32_e32 v75, 0x41800000, v75
	v_med3_f32 v74, v74, s17, v147
	v_med3_f32 v75, v75, s17, v147
	v_cvt_pk_fp8_f32 v91, v74, v75
	v_pk_fma_f32 v[76:77], v[124:125], v[76:77], v[116:117]
	s_nop 0
	v_mul_f32_e32 v76, 0x41800000, v76
	v_mul_f32_e32 v74, 0x41800000, v77
	v_med3_f32 v75, v76, s17, v147
	v_med3_f32 v74, v74, s17, v147
	v_cvt_pk_fp8_f32 v91, v75, v74 op_sel:[0,0,1]
	s_nop 0
	v_pk_mul_f32 v[74:75], v[90:91], v[106:107] op_sel_hi:[0,1]
	s_waitcnt lgkmcnt(0)
	v_pk_fma_f32 v[74:75], v[74:75], v[110:111], v[118:119]
	v_mov_b32_e32 v118, 0
	v_mul_f32_e32 v74, 0x41800000, v74
	v_mul_f32_e32 v75, 0x41800000, v75
	v_med3_f32 v74, v74, s17, v147
	v_med3_f32 v75, v75, s17, v147
	v_pk_mul_f32 v[76:77], v[90:91], v[108:109] op_sel_hi:[0,1]
	v_cvt_pk_fp8_f32 v118, v74, v75
	v_pk_fma_f32 v[76:77], v[76:77], v[112:113], v[120:121]
	v_pk_mul_f32 v[114:115], v[90:91], v[102:103] op_sel_hi:[0,1]
	v_mul_f32_e32 v76, 0x41800000, v76
	v_mul_f32_e32 v74, 0x41800000, v77
	v_med3_f32 v75, v76, s17, v147
	v_med3_f32 v74, v74, s17, v147
	v_cvt_pk_fp8_f32 v118, v75, v74 op_sel:[0,0,1]
	ds_read_b128 v[74:77], v1 offset:10240
	ds_read_b128 v[106:109], v1 offset:26624
	v_pk_mul_f32 v[116:117], v[90:91], v[104:105] op_sel_hi:[0,1]
	ds_read_b128 v[102:105], v1 offset:11264
	ds_read_b128 v[110:113], v1 offset:27648
	s_waitcnt lgkmcnt(2)
	v_pk_fma_f32 v[74:75], v[114:115], v[74:75], v[106:107]
	s_nop 0
	v_mul_f32_e32 v74, 0x41800000, v74
	v_mul_f32_e32 v75, 0x41800000, v75
	v_med3_f32 v74, v74, s17, v147
	v_med3_f32 v75, v75, s17, v147
	v_mov_b32_e32 v106, 0
	v_cvt_pk_fp8_f32 v106, v74, v75
	v_pk_fma_f32 v[76:77], v[116:117], v[76:77], v[108:109]
	v_pk_mul_f32 v[108:109], v[90:91], v[96:97] op_sel_hi:[0,1]
	v_mul_f32_e32 v76, 0x41800000, v76
	v_mul_f32_e32 v74, 0x41800000, v77
	v_med3_f32 v75, v76, s17, v147
	v_med3_f32 v74, v74, s17, v147
	v_cvt_pk_fp8_f32 v106, v75, v74 op_sel:[0,0,1]
	v_pk_mul_f32 v[74:75], v[90:91], v[98:99] op_sel_hi:[0,1]
	s_waitcnt lgkmcnt(0)
	v_pk_fma_f32 v[74:75], v[74:75], v[102:103], v[110:111]
	v_mov_b32_e32 v98, 0
	v_mul_f32_e32 v74, 0x41800000, v74
	v_mul_f32_e32 v75, 0x41800000, v75
	v_med3_f32 v74, v74, s17, v147
	v_med3_f32 v75, v75, s17, v147
	v_pk_mul_f32 v[76:77], v[90:91], v[100:101] op_sel_hi:[0,1]
	v_cvt_pk_fp8_f32 v98, v74, v75
	v_pk_fma_f32 v[76:77], v[76:77], v[104:105], v[112:113]
	s_nop 0
	v_mul_f32_e32 v76, 0x41800000, v76
	v_mul_f32_e32 v74, 0x41800000, v77
	v_med3_f32 v75, v76, s17, v147
	v_med3_f32 v74, v74, s17, v147
	v_cvt_pk_fp8_f32 v98, v75, v74 op_sel:[0,0,1]
	global_store_dword v[88:89], v91, off offset:2048
	global_store_dword v[88:89], v118, off offset:2304
	global_store_dword v[88:89], v106, off offset:2560
	global_store_dword v[88:89], v98, off offset:2816
	ds_read_b128 v[74:77], v1 offset:12288
	ds_read_b128 v[98:101], v1 offset:28672
	v_pk_mul_f32 v[106:107], v[90:91], v[94:95] op_sel_hi:[0,1]
	v_mov_b32_e32 v91, 0
	ds_read_b128 v[94:97], v1 offset:13312
	ds_read_b128 v[102:105], v1 offset:14336
	s_waitcnt lgkmcnt(2)
	v_pk_fma_f32 v[74:75], v[106:107], v[74:75], v[98:99]
	s_nop 0
	v_mul_f32_e32 v74, 0x41800000, v74
	v_mul_f32_e32 v75, 0x41800000, v75
	v_med3_f32 v74, v74, s17, v147
	v_med3_f32 v75, v75, s17, v147
	v_cvt_pk_fp8_f32 v91, v74, v75
	v_pk_fma_f32 v[76:77], v[108:109], v[76:77], v[100:101]
	s_nop 0
	v_mul_f32_e32 v76, 0x41800000, v76
	v_mul_f32_e32 v77, 0x41800000, v77
	v_med3_f32 v98, v76, s17, v147
	v_med3_f32 v99, v77, s17, v147
	ds_read_b128 v[74:77], v1 offset:29696
	v_cvt_pk_fp8_f32 v91, v98, v99 op_sel:[0,0,1]
	ds_read_b128 v[98:101], v1 offset:30720
	v_pk_mul_f32 v[86:87], v[90:91], v[86:87] op_sel_hi:[0,1]
	s_waitcnt lgkmcnt(1)
	v_pk_fma_f32 v[74:75], v[86:87], v[94:95], v[74:75]
	v_mov_b32_e32 v86, 0
	v_mul_f32_e32 v74, 0x41800000, v74
	v_mul_f32_e32 v75, 0x41800000, v75
	v_med3_f32 v74, v74, s17, v147
	v_med3_f32 v75, v75, s17, v147
	v_pk_mul_f32 v[92:93], v[90:91], v[92:93] op_sel_hi:[0,1]
	v_cvt_pk_fp8_f32 v86, v74, v75
	v_pk_fma_f32 v[76:77], v[92:93], v[96:97], v[76:77]
	v_mov_b32_e32 v92, 0
	v_mul_f32_e32 v76, 0x41800000, v76
	v_mul_f32_e32 v74, 0x41800000, v77
	v_med3_f32 v75, v76, s17, v147
	v_med3_f32 v74, v74, s17, v147
	v_cvt_pk_fp8_f32 v86, v75, v74 op_sel:[0,0,1]
	v_pk_mul_f32 v[74:75], v[90:91], v[82:83] op_sel_hi:[0,1]
	v_pk_mul_f32 v[76:77], v[90:91], v[84:85] op_sel_hi:[0,1]
	s_waitcnt lgkmcnt(0)
	v_pk_fma_f32 v[74:75], v[74:75], v[102:103], v[98:99]
	v_pk_fma_f32 v[76:77], v[76:77], v[104:105], v[100:101]
	v_mul_f32_e32 v74, 0x41800000, v74
	v_mul_f32_e32 v75, 0x41800000, v75
	v_mul_f32_e32 v76, 0x41800000, v76
	v_med3_f32 v74, v74, s17, v147
	v_med3_f32 v75, v75, s17, v147
	v_mul_f32_e32 v87, 0x41800000, v77
	v_cvt_pk_fp8_f32 v92, v74, v75
	v_med3_f32 v93, v76, s17, v147
	ds_read_b128 v[74:77], v142
	ds_read_b128 v[82:85], v142 offset:16384
	v_pk_mul_f32 v[78:79], v[90:91], v[78:79] op_sel_hi:[0,1]
	v_pk_mul_f32 v[80:81], v[90:91], v[80:81] op_sel_hi:[0,1]
	v_med3_f32 v87, v87, s17, v147
	v_cvt_pk_fp8_f32 v92, v93, v87 op_sel:[0,0,1]
	s_waitcnt lgkmcnt(0)
	v_pk_fma_f32 v[74:75], v[78:79], v[74:75], v[82:83]
	v_mov_b32_e32 v78, 0
	v_mul_f32_e32 v74, 0x41800000, v74
	v_mul_f32_e32 v75, 0x41800000, v75
	v_med3_f32 v74, v74, s17, v147
	v_med3_f32 v75, v75, s17, v147
	v_cvt_pk_fp8_f32 v78, v74, v75
	v_pk_fma_f32 v[76:77], v[80:81], v[76:77], v[84:85]
	s_nop 0
	v_mul_f32_e32 v76, 0x41800000, v76
	v_mul_f32_e32 v74, 0x41800000, v77
	v_med3_f32 v75, v76, s17, v147
	v_med3_f32 v74, v74, s17, v147
	v_cvt_pk_fp8_f32 v78, v75, v74 op_sel:[0,0,1]
	v_mul_f32_e32 v74, v71, v71
	v_mul_f32_e32 v75, v73, v73
	v_fmac_f32_e32 v74, v70, v70
	v_fmac_f32_e32 v75, v72, v72
	v_add_f32_e32 v74, v74, v75
	v_mul_f32_e32 v75, v67, v67
	v_mul_f32_e32 v76, v69, v69
	v_fmac_f32_e32 v75, v66, v66
	v_fmac_f32_e32 v76, v68, v68
	v_add_f32_e32 v75, v75, v76
	v_add_f32_e32 v74, v74, v75
	v_mul_f32_e32 v75, v63, v63
	v_mul_f32_e32 v76, v65, v65
	v_fmac_f32_e32 v75, v62, v62
	v_fmac_f32_e32 v76, v64, v64
	v_add_f32_e32 v75, v75, v76
	v_add_f32_e32 v74, v74, v75
	v_mul_f32_e32 v75, v59, v59
	v_mul_f32_e32 v76, v61, v61
	v_fmac_f32_e32 v75, v58, v58
	v_fmac_f32_e32 v76, v60, v60
	v_add_f32_e32 v75, v75, v76
	v_add_f32_e32 v74, v74, v75
	v_mul_f32_e32 v75, v55, v55
	v_mul_f32_e32 v76, v57, v57
	v_fmac_f32_e32 v75, v54, v54
	v_fmac_f32_e32 v76, v56, v56
	v_add_f32_e32 v75, v75, v76
	v_add_f32_e32 v74, v74, v75
	v_mul_f32_e32 v75, v51, v51
	v_mul_f32_e32 v76, v53, v53
	v_fmac_f32_e32 v75, v50, v50
	v_fmac_f32_e32 v76, v52, v52
	v_add_f32_e32 v75, v75, v76
	v_add_f32_e32 v74, v74, v75
	v_mul_f32_e32 v75, v47, v47
	v_mul_f32_e32 v76, v49, v49
	v_fmac_f32_e32 v75, v46, v46
	v_fmac_f32_e32 v76, v48, v48
	v_add_f32_e32 v75, v75, v76
	v_add_f32_e32 v74, v74, v75
	v_mul_f32_e32 v75, v43, v43
	v_mul_f32_e32 v76, v45, v45
	v_fmac_f32_e32 v75, v42, v42
	v_fmac_f32_e32 v76, v44, v44
	v_add_f32_e32 v75, v75, v76
	v_add_f32_e32 v74, v74, v75
	v_mul_f32_e32 v75, v39, v39
	v_mul_f32_e32 v76, v41, v41
	v_fmac_f32_e32 v75, v38, v38
	v_fmac_f32_e32 v76, v40, v40
	v_add_f32_e32 v75, v75, v76
	v_add_f32_e32 v74, v74, v75
	v_mul_f32_e32 v75, v35, v35
	v_mul_f32_e32 v76, v37, v37
	v_fmac_f32_e32 v75, v34, v34
	v_fmac_f32_e32 v76, v36, v36
	v_add_f32_e32 v75, v75, v76
	v_add_f32_e32 v74, v74, v75
	v_mul_f32_e32 v75, v29, v29
	v_mul_f32_e32 v76, v31, v31
	v_fmac_f32_e32 v75, v28, v28
	v_fmac_f32_e32 v76, v30, v30
	v_add_f32_e32 v75, v75, v76
	v_add_f32_e32 v74, v74, v75
	v_mul_f32_e32 v75, v21, v21
	v_mul_f32_e32 v76, v23, v23
	v_fmac_f32_e32 v75, v20, v20
	v_fmac_f32_e32 v76, v22, v22
	v_add_f32_e32 v75, v75, v76
	v_add_f32_e32 v74, v74, v75
	v_mul_f32_e32 v75, v17, v17
	v_mul_f32_e32 v76, v19, v19
	v_fmac_f32_e32 v75, v16, v16
	v_fmac_f32_e32 v76, v18, v18
	v_add_f32_e32 v75, v75, v76
	v_add_f32_e32 v74, v74, v75
	v_mul_f32_e32 v75, v13, v13
	v_mul_f32_e32 v76, v15, v15
	v_fmac_f32_e32 v75, v12, v12
	v_fmac_f32_e32 v76, v14, v14
	v_add_f32_e32 v75, v75, v76
	v_add_f32_e32 v74, v74, v75
	v_mul_f32_e32 v75, v11, v11
	v_mul_f32_e32 v76, v33, v33
	v_fmac_f32_e32 v75, v10, v10
	v_fmac_f32_e32 v76, v32, v32
	v_add_f32_e32 v75, v75, v76
	v_add_f32_e32 v74, v74, v75
	v_mul_f32_e32 v75, v25, v25
	v_mul_f32_e32 v76, v27, v27
	v_fmac_f32_e32 v75, v24, v24
	v_fmac_f32_e32 v76, v26, v26
	v_add_f32_e32 v75, v75, v76
	v_add_f32_e32 v74, v74, v75
	global_store_dword v[88:89], v91, off offset:3072
	global_store_dword v[88:89], v86, off offset:3328
	global_store_dword v[88:89], v92, off offset:3584
	global_store_dword v[88:89], v78, off offset:3840
	v_add_f32_dpp v74, v74, v74 quad_perm:[1,0,3,2] row_mask:0xf bank_mask:0xf bound_ctrl:1
	s_nop 1
	v_add_f32_dpp v74, v74, v74 quad_perm:[2,3,0,1] row_mask:0xf bank_mask:0xf bound_ctrl:1
	s_nop 1
	v_add_f32_dpp v74, v74, v74 row_half_mirror row_mask:0xf bank_mask:0xf bound_ctrl:1
	s_nop 1
	v_add_f32_dpp v74, v74, v74 row_mirror row_mask:0xf bank_mask:0xf bound_ctrl:1
	v_mov_b32_e32 v75, v74
	s_nop 1
	v_permlane16_swap_b32 v74, v75
	s_nop 0
	v_add_f32_e32 v74, v74, v75
	v_mov_b32_e32 v75, v74
	s_nop 1
	v_permlane32_swap_b32 v74, v75
	s_nop 0
	v_add_f32_e32 v74, v74, v75
	v_fmamk_f32 v74, v74, 0x39800000, v145
	v_mul_f32_e32 v75, 0x4f800000, v74
	v_cmp_gt_f32_e32 vcc, s16, v74
	s_nop 1
	v_cndmask_b32_e32 v74, v74, v75, vcc
	v_sqrt_f32_e32 v75, v74
	s_nop 0
	v_add_u32_e32 v76, -1, v75
	v_fma_f32 v77, -v76, v75, v74
	v_cmp_ge_f32_e64 s[0:1], 0, v77
	v_add_u32_e32 v77, 1, v75
	s_nop 0
	v_cndmask_b32_e64 v76, v75, v76, s[0:1]
	v_fma_f32 v75, -v77, v75, v74
	v_cmp_lt_f32_e64 s[0:1], 0, v75
	s_nop 1
	v_cndmask_b32_e64 v75, v76, v77, s[0:1]
	v_mul_f32_e32 v76, 0x37800000, v75
	v_cndmask_b32_e32 v75, v75, v76, vcc
	v_cmp_class_f32_e32 vcc, v74, v146
	s_nop 1
	v_cndmask_b32_e32 v74, v75, v74, vcc
	v_div_scale_f32 v75, s[0:1], v74, v74, 1.0
	v_rcp_f32_e32 v76, v75
	s_lshl_b64 s[0:1], s[8:9], 12
	s_cmpk_gt_i32 s18, 0xff
	v_fma_f32 v77, -v75, v76, 1.0
	v_fmac_f32_e32 v76, v77, v76
	v_div_scale_f32 v77, vcc, 1.0, v74, 1.0
	v_mul_f32_e32 v78, v77, v76
	v_fma_f32 v79, -v75, v78, v77
	v_fmac_f32_e32 v78, v79, v76
	v_fma_f32 v75, -v75, v78, v77
	v_div_fmas_f32 v75, v75, v76, v78
	ds_read_b128 v[78:81], v1
	ds_read_b128 v[82:85], v1 offset:16384
	v_div_fixup_f32 v76, v75, v74, 1.0
	v_pk_mul_f32 v[90:91], v[76:77], v[70:71] op_sel_hi:[0,1]
	v_pk_mul_f32 v[92:93], v[76:77], v[72:73] op_sel_hi:[0,1]
	ds_read_b128 v[70:73], v1 offset:1024
	ds_read_b128 v[86:89], v1 offset:17408
	s_waitcnt lgkmcnt(2)
	v_pk_fma_f32 v[78:79], v[78:79], v[90:91], v[82:83]
	v_pk_fma_f32 v[80:81], v[80:81], v[92:93], v[84:85]
	v_mul_f32_e32 v77, 0x41800000, v78
	v_mul_f32_e32 v78, 0x41800000, v79
	v_med3_f32 v77, v77, s17, v147
	v_med3_f32 v78, v78, s17, v147
	v_mov_b32_e32 v90, 0
	v_cvt_pk_fp8_f32 v90, v77, v78
	v_mul_f32_e32 v77, 0x41800000, v81
	v_med3_f32 v77, v77, s17, v147
	v_pk_mul_f32 v[66:67], v[76:77], v[66:67] op_sel_hi:[0,1]
	v_mul_f32_e32 v79, 0x41800000, v80
	s_waitcnt lgkmcnt(0)
	v_pk_fma_f32 v[66:67], v[70:71], v[66:67], v[86:87]
	v_med3_f32 v78, v79, s17, v147
	v_mul_f32_e32 v66, 0x41800000, v66
	v_mul_f32_e32 v67, 0x41800000, v67
	v_cvt_pk_fp8_f32 v90, v78, v77 op_sel:[0,0,1]
	v_pk_mul_f32 v[68:69], v[76:77], v[68:69] op_sel_hi:[0,1]
	v_med3_f32 v66, v66, s17, v147
	v_med3_f32 v67, v67, s17, v147
	v_mov_b32_e32 v77, 0
	v_cvt_pk_fp8_f32 v77, v66, v67
	v_pk_fma_f32 v[68:69], v[72:73], v[68:69], v[88:89]
	v_lshl_add_u64 v[74:75], v[4:5], 0, s[0:1]
	v_mul_f32_e32 v68, 0x41800000, v68
	v_mul_f32_e32 v66, 0x41800000, v69
	v_med3_f32 v67, v68, s17, v147
	v_med3_f32 v66, v66, s17, v147
	v_cvt_pk_fp8_f32 v77, v67, v66 op_sel:[0,0,1]
	ds_read_b128 v[66:69], v1 offset:2048
	ds_read_b128 v[70:73], v1 offset:18432
	v_pk_mul_f32 v[82:83], v[76:77], v[62:63] op_sel_hi:[0,1]
	v_pk_mul_f32 v[84:85], v[76:77], v[64:65] op_sel_hi:[0,1]
	ds_read_b128 v[62:65], v1 offset:3072
	ds_read_b128 v[78:81], v1 offset:19456
	s_waitcnt lgkmcnt(2)
	v_pk_fma_f32 v[66:67], v[82:83], v[66:67], v[70:71]
	v_pk_mul_f32 v[58:59], v[76:77], v[58:59] op_sel_hi:[0,1]
	v_mul_f32_e32 v66, 0x41800000, v66
	v_mul_f32_e32 v67, 0x41800000, v67
	s_waitcnt lgkmcnt(0)
	v_pk_fma_f32 v[58:59], v[58:59], v[62:63], v[78:79]
	v_med3_f32 v66, v66, s17, v147
	v_med3_f32 v67, v67, s17, v147
	v_mov_b32_e32 v70, 0
	v_mul_f32_e32 v58, 0x41800000, v58
	v_mul_f32_e32 v59, 0x41800000, v59
	v_cvt_pk_fp8_f32 v70, v66, v67
	v_med3_f32 v58, v58, s17, v147
	v_med3_f32 v59, v59, s17, v147
	v_mov_b32_e32 v62, 0
	v_pk_fma_f32 v[68:69], v[84:85], v[68:69], v[72:73]
	v_pk_mul_f32 v[60:61], v[76:77], v[60:61] op_sel_hi:[0,1]
	v_cvt_pk_fp8_f32 v62, v58, v59
	v_mul_f32_e32 v68, 0x41800000, v68
	v_mul_f32_e32 v66, 0x41800000, v69
	v_pk_fma_f32 v[60:61], v[60:61], v[64:65], v[80:81]
	v_med3_f32 v67, v68, s17, v147
	v_med3_f32 v66, v66, s17, v147
	v_mul_f32_e32 v60, 0x41800000, v60
	v_mul_f32_e32 v58, 0x41800000, v61
	v_cvt_pk_fp8_f32 v70, v67, v66 op_sel:[0,0,1]
	v_med3_f32 v59, v60, s17, v147
	v_med3_f32 v58, v58, s17, v147
	v_cvt_pk_fp8_f32 v62, v59, v58 op_sel:[0,0,1]
	global_store_dword v[74:75], v90, off
	global_store_dword v[74:75], v77, off offset:256
	global_store_dword v[74:75], v70, off offset:512
	global_store_dword v[74:75], v62, off offset:768
	ds_read_b128 v[58:61], v1 offset:4096
	ds_read_b128 v[62:65], v1 offset:20480
	v_pk_mul_f32 v[70:71], v[76:77], v[54:55] op_sel_hi:[0,1]
	v_pk_mul_f32 v[72:73], v[76:77], v[56:57] op_sel_hi:[0,1]
	ds_read_b128 v[54:57], v1 offset:5120
	ds_read_b128 v[66:69], v1 offset:21504
	v_pk_mul_f32 v[50:51], v[76:77], v[50:51] op_sel_hi:[0,1]
	s_waitcnt lgkmcnt(2)
	v_pk_fma_f32 v[58:59], v[70:71], v[58:59], v[62:63]
	v_mov_b32_e32 v70, 0
	v_mul_f32_e32 v58, 0x41800000, v58
	s_waitcnt lgkmcnt(0)
	v_pk_fma_f32 v[50:51], v[50:51], v[54:55], v[66:67]
	v_mul_f32_e32 v59, 0x41800000, v59
	v_mul_f32_e32 v50, 0x41800000, v50
	v_mul_f32_e32 v51, 0x41800000, v51
	v_med3_f32 v50, v50, s17, v147
	v_med3_f32 v51, v51, s17, v147
	v_mov_b32_e32 v66, 0
	v_med3_f32 v58, v58, s17, v147
	v_med3_f32 v59, v59, s17, v147
	v_pk_mul_f32 v[52:53], v[76:77], v[52:53] op_sel_hi:[0,1]
	v_cvt_pk_fp8_f32 v66, v50, v51
	v_cvt_pk_fp8_f32 v70, v58, v59
	v_pk_fma_f32 v[52:53], v[52:53], v[56:57], v[68:69]
	v_pk_fma_f32 v[60:61], v[72:73], v[60:61], v[64:65]
	v_mul_f32_e32 v52, 0x41800000, v52
	v_mul_f32_e32 v50, 0x41800000, v53
	v_mul_f32_e32 v60, 0x41800000, v60
	v_mul_f32_e32 v58, 0x41800000, v61
	v_med3_f32 v51, v52, s17, v147
	v_med3_f32 v50, v50, s17, v147
	v_med3_f32 v59, v60, s17, v147
	v_med3_f32 v58, v58, s17, v147
	v_cvt_pk_fp8_f32 v66, v51, v50 op_sel:[0,0,1]
	ds_read_b128 v[50:53], v1 offset:6144
	ds_read_b128 v[54:57], v1 offset:22528
	v_cvt_pk_fp8_f32 v70, v59, v58 op_sel:[0,0,1]
	v_pk_mul_f32 v[62:63], v[76:77], v[46:47] op_sel_hi:[0,1]
	v_pk_mul_f32 v[64:65], v[76:77], v[48:49] op_sel_hi:[0,1]
	ds_read_b128 v[46:49], v1 offset:7168
	ds_read_b128 v[58:61], v1 offset:23552
	s_waitcnt lgkmcnt(2)
	v_pk_fma_f32 v[50:51], v[62:63], v[50:51], v[54:55]
	v_pk_mul_f32 v[42:43], v[76:77], v[42:43] op_sel_hi:[0,1]
	v_mul_f32_e32 v50, 0x41800000, v50
	v_mul_f32_e32 v51, 0x41800000, v51
	s_waitcnt lgkmcnt(0)
	v_pk_fma_f32 v[42:43], v[42:43], v[46:47], v[58:59]
	v_med3_f32 v50, v50, s17, v147
	v_med3_f32 v51, v51, s17, v147
	v_mov_b32_e32 v54, 0
	v_mul_f32_e32 v42, 0x41800000, v42
	v_mul_f32_e32 v43, 0x41800000, v43
	v_cvt_pk_fp8_f32 v54, v50, v51
	v_med3_f32 v42, v42, s17, v147
	v_med3_f32 v43, v43, s17, v147
	v_mov_b32_e32 v46, 0
	v_pk_fma_f32 v[52:53], v[64:65], v[52:53], v[56:57]
	v_pk_mul_f32 v[44:45], v[76:77], v[44:45] op_sel_hi:[0,1]
	v_cvt_pk_fp8_f32 v46, v42, v43
	v_mul_f32_e32 v52, 0x41800000, v52
	v_mul_f32_e32 v50, 0x41800000, v53
	v_pk_fma_f32 v[44:45], v[44:45], v[48:49], v[60:61]
	v_med3_f32 v51, v52, s17, v147
	v_med3_f32 v50, v50, s17, v147
	v_mul_f32_e32 v44, 0x41800000, v44
	v_mul_f32_e32 v42, 0x41800000, v45
	v_cvt_pk_fp8_f32 v54, v51, v50 op_sel:[0,0,1]
	v_med3_f32 v43, v44, s17, v147
	v_med3_f32 v42, v42, s17, v147
	v_cvt_pk_fp8_f32 v46, v43, v42 op_sel:[0,0,1]
	global_store_dword v[74:75], v70, off offset:1024
	global_store_dword v[74:75], v66, off offset:1280
	global_store_dword v[74:75], v54, off offset:1536
	global_store_dword v[74:75], v46, off offset:1792
	ds_read_b128 v[42:45], v1 offset:8192
	ds_read_b128 v[46:49], v1 offset:24576
	v_pk_mul_f32 v[54:55], v[76:77], v[38:39] op_sel_hi:[0,1]
	v_pk_mul_f32 v[56:57], v[76:77], v[40:41] op_sel_hi:[0,1]
	ds_read_b128 v[38:41], v1 offset:9216
	ds_read_b128 v[50:53], v1 offset:25600
	v_pk_mul_f32 v[34:35], v[76:77], v[34:35] op_sel_hi:[0,1]
	s_waitcnt lgkmcnt(2)
;     ...
;     for (int blk = blockIdx.x; blk < M / 32; blk += F.G) {
;     ...
;         NR_LOAD(va, m0); NR_LOAD(vb, m0 + 1); NR_FIN(va, m0); NR_LOAD(va, m0 + 2); NR_FIN(vb, m0 + 1); NR_LOAD(vb, m0 + 3); NR_FIN(va, m0 + 2); NR_FIN(vb, m0 + 3);
	v_pk_fma_f32 v[42:43], v[54:55], v[42:43], v[46:47]
	v_mov_b32_e32 v54, 0
	v_mul_f32_e32 v42, 0x41800000, v42
	s_waitcnt lgkmcnt(0)
	v_pk_fma_f32 v[34:35], v[34:35], v[38:39], v[50:51]
	v_mul_f32_e32 v43, 0x41800000, v43
	v_mul_f32_e32 v34, 0x41800000, v34
	v_mul_f32_e32 v35, 0x41800000, v35
	v_med3_f32 v34, v34, s17, v147
	v_med3_f32 v35, v35, s17, v147
	v_mov_b32_e32 v50, 0
	v_med3_f32 v42, v42, s17, v147
	v_med3_f32 v43, v43, s17, v147
	v_pk_mul_f32 v[36:37], v[76:77], v[36:37] op_sel_hi:[0,1]
	v_cvt_pk_fp8_f32 v50, v34, v35
	v_cvt_pk_fp8_f32 v54, v42, v43
	v_pk_fma_f32 v[36:37], v[36:37], v[40:41], v[52:53]
	v_pk_fma_f32 v[44:45], v[56:57], v[44:45], v[48:49]
	v_mul_f32_e32 v36, 0x41800000, v36
	v_mul_f32_e32 v34, 0x41800000, v37
	v_mul_f32_e32 v44, 0x41800000, v44
	v_mul_f32_e32 v42, 0x41800000, v45
	v_med3_f32 v35, v36, s17, v147
	v_med3_f32 v34, v34, s17, v147
	v_med3_f32 v43, v44, s17, v147
	v_med3_f32 v42, v42, s17, v147
	v_cvt_pk_fp8_f32 v50, v35, v34 op_sel:[0,0,1]
	ds_read_b128 v[34:37], v1 offset:10240
	ds_read_b128 v[38:41], v1 offset:26624
	v_cvt_pk_fp8_f32 v54, v43, v42 op_sel:[0,0,1]
	v_pk_mul_f32 v[46:47], v[76:77], v[28:29] op_sel_hi:[0,1]
	v_pk_mul_f32 v[48:49], v[76:77], v[30:31] op_sel_hi:[0,1]
	ds_read_b128 v[28:31], v1 offset:11264
	ds_read_b128 v[42:45], v1 offset:27648
	s_waitcnt lgkmcnt(2)
	v_pk_fma_f32 v[34:35], v[46:47], v[34:35], v[38:39]
	v_pk_mul_f32 v[20:21], v[76:77], v[20:21] op_sel_hi:[0,1]
	v_mul_f32_e32 v34, 0x41800000, v34
	v_mul_f32_e32 v35, 0x41800000, v35
	s_waitcnt lgkmcnt(0)
	v_pk_fma_f32 v[20:21], v[20:21], v[28:29], v[42:43]
	v_med3_f32 v34, v34, s17, v147
	v_med3_f32 v35, v35, s17, v147
	v_mov_b32_e32 v38, 0
	v_mul_f32_e32 v20, 0x41800000, v20
	v_mul_f32_e32 v21, 0x41800000, v21
	v_cvt_pk_fp8_f32 v38, v34, v35
	v_med3_f32 v20, v20, s17, v147
	v_med3_f32 v21, v21, s17, v147
	v_mov_b32_e32 v28, 0
	v_pk_fma_f32 v[36:37], v[48:49], v[36:37], v[40:41]
	v_pk_mul_f32 v[22:23], v[76:77], v[22:23] op_sel_hi:[0,1]
	v_cvt_pk_fp8_f32 v28, v20, v21
	v_mul_f32_e32 v36, 0x41800000, v36
	v_mul_f32_e32 v34, 0x41800000, v37
	v_pk_fma_f32 v[22:23], v[22:23], v[30:31], v[44:45]
	v_med3_f32 v35, v36, s17, v147
	v_med3_f32 v34, v34, s17, v147
	v_mul_f32_e32 v22, 0x41800000, v22
	v_mul_f32_e32 v20, 0x41800000, v23
	v_cvt_pk_fp8_f32 v38, v35, v34 op_sel:[0,0,1]
	v_med3_f32 v21, v22, s17, v147
	v_med3_f32 v20, v20, s17, v147
	v_cvt_pk_fp8_f32 v28, v21, v20 op_sel:[0,0,1]
	global_store_dword v[74:75], v54, off offset:2048
	global_store_dword v[74:75], v50, off offset:2304
	global_store_dword v[74:75], v38, off offset:2560
	global_store_dword v[74:75], v28, off offset:2816
	ds_read_b128 v[20:23], v1 offset:12288
	ds_read_b128 v[28:31], v1 offset:28672
	v_pk_mul_f32 v[38:39], v[76:77], v[16:17] op_sel_hi:[0,1]
	v_pk_mul_f32 v[40:41], v[76:77], v[18:19] op_sel_hi:[0,1]
	ds_read_b128 v[16:19], v1 offset:13312
	ds_read_b128 v[34:37], v1 offset:14336
	v_pk_mul_f32 v[10:11], v[76:77], v[10:11] op_sel_hi:[0,1]
	s_waitcnt lgkmcnt(2)
	v_pk_fma_f32 v[20:21], v[38:39], v[20:21], v[28:29]
	v_pk_fma_f32 v[22:23], v[40:41], v[22:23], v[30:31]
	v_mul_f32_e32 v20, 0x41800000, v20
	v_mul_f32_e32 v21, 0x41800000, v21
	v_mul_f32_e32 v22, 0x41800000, v22
	v_mul_f32_e32 v23, 0x41800000, v23
	v_med3_f32 v20, v20, s17, v147
	v_med3_f32 v21, v21, s17, v147
	v_mov_b32_e32 v38, 0
	v_cvt_pk_fp8_f32 v38, v20, v21
	v_med3_f32 v28, v22, s17, v147
	v_med3_f32 v29, v23, s17, v147
	ds_read_b128 v[20:23], v1 offset:29696
	v_cvt_pk_fp8_f32 v38, v28, v29 op_sel:[0,0,1]
	v_pk_mul_f32 v[28:29], v[76:77], v[12:13] op_sel_hi:[0,1]
	v_pk_mul_f32 v[30:31], v[76:77], v[14:15] op_sel_hi:[0,1]
	ds_read_b128 v[12:15], v1 offset:30720
	s_waitcnt lgkmcnt(1)
	v_pk_fma_f32 v[16:17], v[28:29], v[16:17], v[20:21]
	v_pk_fma_f32 v[18:19], v[30:31], v[18:19], v[22:23]
	v_mul_f32_e32 v16, 0x41800000, v16
	v_mul_f32_e32 v17, 0x41800000, v17
	v_med3_f32 v16, v16, s17, v147
	v_med3_f32 v17, v17, s17, v147
	v_mov_b32_e32 v22, 0
	v_cvt_pk_fp8_f32 v22, v16, v17
	v_mul_f32_e32 v18, 0x41800000, v18
	v_mul_f32_e32 v16, 0x41800000, v19
	v_med3_f32 v17, v18, s17, v147
	v_med3_f32 v16, v16, s17, v147
	v_cvt_pk_fp8_f32 v22, v17, v16 op_sel:[0,0,1]
	v_pk_mul_f32 v[16:17], v[76:77], v[32:33] op_sel_hi:[0,1]
	s_waitcnt lgkmcnt(0)
	v_pk_fma_f32 v[10:11], v[10:11], v[34:35], v[12:13]
	v_pk_fma_f32 v[14:15], v[16:17], v[36:37], v[14:15]
	v_mul_f32_e32 v10, 0x41800000, v10
	v_mul_f32_e32 v11, 0x41800000, v11
	v_mul_f32_e32 v12, 0x41800000, v14
	v_med3_f32 v10, v10, s17, v147
	v_med3_f32 v11, v11, s17, v147
	v_mov_b32_e32 v23, 0
	v_mul_f32_e32 v18, 0x41800000, v15
	v_cvt_pk_fp8_f32 v23, v10, v11
	v_med3_f32 v19, v12, s17, v147
	ds_read_b128 v[10:13], v142
	ds_read_b128 v[14:17], v142 offset:16384
	v_med3_f32 v18, v18, s17, v147
	v_cvt_pk_fp8_f32 v23, v19, v18 op_sel:[0,0,1]
	v_pk_mul_f32 v[18:19], v[76:77], v[24:25] op_sel_hi:[0,1]
	v_pk_mul_f32 v[20:21], v[76:77], v[26:27] op_sel_hi:[0,1]
	s_waitcnt lgkmcnt(0)
	v_pk_fma_f32 v[10:11], v[18:19], v[10:11], v[14:15]
	v_mov_b32_e32 v14, 0
	v_mul_f32_e32 v10, 0x41800000, v10
	v_mul_f32_e32 v11, 0x41800000, v11
	v_med3_f32 v10, v10, s17, v147
	v_med3_f32 v11, v11, s17, v147
	v_cvt_pk_fp8_f32 v14, v10, v11
	v_pk_fma_f32 v[12:13], v[20:21], v[12:13], v[16:17]
	s_nop 0
	v_mul_f32_e32 v12, 0x41800000, v12
	v_mul_f32_e32 v10, 0x41800000, v13
	v_med3_f32 v11, v12, s17, v147
	v_med3_f32 v10, v10, s17, v147
	v_cvt_pk_fp8_f32 v14, v11, v10 op_sel:[0,0,1]
	global_store_dword v[74:75], v38, off offset:3072
	global_store_dword v[74:75], v22, off offset:3328
	global_store_dword v[74:75], v23, off offset:3584
	global_store_dword v[74:75], v14, off offset:3840
	s_cbranch_scc0 .LBB0_2291
